# all four big GEMM phases: epilogue stores of each workgroup's last tile are write-through (sc1) to shorten the XCD leader's release write-back at the following grid barrier
# baseline (speedup 1.0000x reference)
.LBB0_985:
	s_lshl_b32 s6, s47, 8
	s_ashr_i32 s7, s6, 31
	s_lshl_b64 s[6:7], s[6:7], 11
	s_lshl_b64 s[0:1], s[0:1], 2
	v_lshl_or_b32 v146, s48, 8, v202
	s_add_u32 s0, s40, s0
	s_addc_u32 s1, s41, s1
	v_ashrrev_i32_e32 v147, 31, v146
	v_lshl_add_u64 v[122:123], v[146:147], 2, s[0:1]
	s_mov_b64 s[0:1], 0x2000
	v_lshl_add_u64 v[126:127], v[122:123], 0, s[0:1]
	s_movk_i32 s0, 0x2000
	v_add_co_u32_e32 v122, vcc, s0, v122
	s_add_u32 s0, s10, s6
	s_addc_u32 s1, s11, s7
	v_lshl_add_u64 v[192:193], v[146:147], 1, s[0:1]
	v_addc_co_u32_e32 v123, vcc, 0, v123, vcc
	v_lshl_add_u64 v[234:235], v[192:193], 0, v[176:177]
	global_load_dwordx4 v[134:137], v[122:123], off
	global_load_dwordx4 v[130:133], v[126:127], off offset:16
	s_nop 0
	global_load_dwordx4 v[122:125], v[126:127], off offset:528
	s_nop 0
	global_load_dwordx4 v[126:129], v[126:127], off offset:512
	s_nop 0
	global_load_dwordx4 v[208:211], v[234:235], off
	global_load_dwordx4 v[212:215], v[234:235], off offset:256
	v_lshl_add_u64 v[198:199], v[192:193], 0, v[178:179]
	global_load_dwordx4 v[230:233], v[198:199], off
	global_load_dwordx4 v[162:165], v[198:199], off offset:256
	v_lshl_add_u64 v[196:197], v[192:193], 0, v[180:181]
	global_load_dwordx4 v[158:161], v[196:197], off
	global_load_dwordx4 v[154:157], v[196:197], off offset:256
	v_lshl_add_u64 v[194:195], v[192:193], 0, v[182:183]
	global_load_dwordx4 v[150:153], v[194:195], off
	global_load_dwordx4 v[146:149], v[194:195], off offset:256
	s_and_b64 vcc, exec, s[4:5]
	s_mov_b32 s48, s16
	s_mov_b32 s47, s46
	s_mov_b64 s[0:1], s[18:19]
	s_mov_b32 s58, 0x800000
	s_movk_i32 s59, 0xe00
	s_waitcnt vmcnt(0)
	v_lshlrev_b32_e32 v236, 16, v208
	v_and_b32_e32 v237, 0xffff0000, v208
	v_lshlrev_b32_e32 v208, 16, v209
	v_and_b32_e32 v209, 0xffff0000, v209
	v_lshlrev_b32_e32 v238, 16, v210
	v_and_b32_e32 v239, 0xffff0000, v210
	v_lshlrev_b32_e32 v210, 16, v211
	v_and_b32_e32 v211, 0xffff0000, v211
	v_pk_fma_f32 v[144:145], v[144:145], v[136:137], v[208:209]
	v_pk_fma_f32 v[142:143], v[142:143], v[134:135], v[236:237]
	v_pk_fma_f32 v[208:209], v[140:141], v[132:133], v[210:211]
	v_pk_fma_f32 v[140:141], v[138:139], v[130:131], v[238:239]
	v_cvt_pk_bf16_f32 v138, v142, v143
	v_cvt_pk_bf16_f32 v139, v144, v145
	v_lshlrev_b32_e32 v142, 16, v214
	v_cvt_pk_bf16_f32 v140, v140, v141
	v_cvt_pk_bf16_f32 v141, v208, v209
	s_cmp_eq_u32 s101, 1
	s_cbranch_scc1 .Lgs1_a_0
	global_store_dwordx4 v[234:235], v[138:141], off
	s_branch .Lgs1_b_0
.Lgs1_a_0:
	global_store_dwordx4 v[234:235], v[138:141], off sc1
.Lgs1_b_0:
	v_and_b32_e32 v143, 0xffff0000, v214
	v_lshlrev_b32_e32 v144, 16, v215
	v_lshlrev_b32_e32 v138, 16, v212
	v_and_b32_e32 v139, 0xffff0000, v212
	v_and_b32_e32 v145, 0xffff0000, v215
	v_lshlrev_b32_e32 v140, 16, v213
	v_and_b32_e32 v141, 0xffff0000, v213
	v_pk_fma_f32 v[118:119], v[118:119], v[126:127], v[138:139]
	v_pk_fma_f32 v[138:139], v[116:117], v[124:125], v[144:145]
	v_pk_fma_f32 v[116:117], v[114:115], v[122:123], v[142:143]
	v_pk_fma_f32 v[120:121], v[120:121], v[128:129], v[140:141]
	v_cvt_pk_bf16_f32 v114, v118, v119
	v_lshlrev_b32_e32 v118, 16, v232
	v_cvt_pk_bf16_f32 v115, v120, v121
	v_cvt_pk_bf16_f32 v116, v116, v117
	v_cvt_pk_bf16_f32 v117, v138, v139
	s_cmp_eq_u32 s101, 1
	s_cbranch_scc1 .Lgs1_a_1
	global_store_dwordx4 v[234:235], v[114:117], off offset:256
	s_branch .Lgs1_b_1
.Lgs1_a_1:
	global_store_dwordx4 v[234:235], v[114:117], off offset:256 sc1
.Lgs1_b_1:
	v_and_b32_e32 v119, 0xffff0000, v232
	v_lshlrev_b32_e32 v120, 16, v233
	v_lshlrev_b32_e32 v114, 16, v230
	v_and_b32_e32 v115, 0xffff0000, v230
	v_lshlrev_b32_e32 v116, 16, v231
	v_and_b32_e32 v117, 0xffff0000, v231
	v_and_b32_e32 v121, 0xffff0000, v233
	v_pk_fma_f32 v[112:113], v[112:113], v[136:137], v[116:117]
	v_pk_fma_f32 v[110:111], v[110:111], v[134:135], v[114:115]
	v_pk_fma_f32 v[114:115], v[108:109], v[132:133], v[120:121]
	v_pk_fma_f32 v[108:109], v[106:107], v[130:131], v[118:119]
	v_cvt_pk_bf16_f32 v106, v110, v111
	v_cvt_pk_bf16_f32 v107, v112, v113
	v_lshlrev_b32_e32 v110, 16, v164
	v_cvt_pk_bf16_f32 v108, v108, v109
	v_cvt_pk_bf16_f32 v109, v114, v115
	s_cmp_eq_u32 s101, 1
	s_cbranch_scc1 .Lgs1_a_2
	global_store_dwordx4 v[198:199], v[106:109], off
	s_branch .Lgs1_b_2
.Lgs1_a_2:
	global_store_dwordx4 v[198:199], v[106:109], off sc1
.Lgs1_b_2:
	v_and_b32_e32 v111, 0xffff0000, v164
	v_lshlrev_b32_e32 v112, 16, v165
	v_lshlrev_b32_e32 v106, 16, v162
	v_and_b32_e32 v107, 0xffff0000, v162
	v_and_b32_e32 v113, 0xffff0000, v165
	v_lshlrev_b32_e32 v108, 16, v163
	v_and_b32_e32 v109, 0xffff0000, v163
	v_pk_fma_f32 v[102:103], v[102:103], v[126:127], v[106:107]
	v_pk_fma_f32 v[106:107], v[100:101], v[124:125], v[112:113]
	v_pk_fma_f32 v[100:101], v[98:99], v[122:123], v[110:111]
	v_pk_fma_f32 v[104:105], v[104:105], v[128:129], v[108:109]
	v_cvt_pk_bf16_f32 v98, v102, v103
	v_lshlrev_b32_e32 v102, 16, v160
	v_cvt_pk_bf16_f32 v99, v104, v105
	v_cvt_pk_bf16_f32 v100, v100, v101
	v_cvt_pk_bf16_f32 v101, v106, v107
	s_cmp_eq_u32 s101, 1
	s_cbranch_scc1 .Lgs1_a_3
	global_store_dwordx4 v[198:199], v[98:101], off offset:256
	s_branch .Lgs1_b_3
.Lgs1_a_3:
	global_store_dwordx4 v[198:199], v[98:101], off offset:256 sc1
.Lgs1_b_3:
	v_and_b32_e32 v103, 0xffff0000, v160
	v_lshlrev_b32_e32 v104, 16, v161
	v_lshlrev_b32_e32 v98, 16, v158
	v_and_b32_e32 v99, 0xffff0000, v158
	v_lshlrev_b32_e32 v100, 16, v159
	v_and_b32_e32 v101, 0xffff0000, v159
	v_and_b32_e32 v105, 0xffff0000, v161
	v_pk_fma_f32 v[96:97], v[96:97], v[136:137], v[100:101]
	v_pk_fma_f32 v[94:95], v[94:95], v[134:135], v[98:99]
	v_pk_fma_f32 v[98:99], v[92:93], v[132:133], v[104:105]
	v_pk_fma_f32 v[92:93], v[90:91], v[130:131], v[102:103]
	v_cvt_pk_bf16_f32 v90, v94, v95
	v_cvt_pk_bf16_f32 v91, v96, v97
	v_lshlrev_b32_e32 v94, 16, v156
	v_cvt_pk_bf16_f32 v92, v92, v93
	v_cvt_pk_bf16_f32 v93, v98, v99
	s_cmp_eq_u32 s101, 1
	s_cbranch_scc1 .Lgs1_a_4
	global_store_dwordx4 v[196:197], v[90:93], off
	s_branch .Lgs1_b_4
.Lgs1_a_4:
	global_store_dwordx4 v[196:197], v[90:93], off sc1
.Lgs1_b_4:
	v_and_b32_e32 v95, 0xffff0000, v156
	v_lshlrev_b32_e32 v96, 16, v157
	v_lshlrev_b32_e32 v90, 16, v154
	v_and_b32_e32 v91, 0xffff0000, v154
	v_and_b32_e32 v97, 0xffff0000, v157
	v_lshlrev_b32_e32 v92, 16, v155
	v_and_b32_e32 v93, 0xffff0000, v155
	v_pk_fma_f32 v[86:87], v[86:87], v[126:127], v[90:91]
	v_pk_fma_f32 v[90:91], v[84:85], v[124:125], v[96:97]
	v_pk_fma_f32 v[84:85], v[82:83], v[122:123], v[94:95]
	v_pk_fma_f32 v[88:89], v[88:89], v[128:129], v[92:93]
	v_cvt_pk_bf16_f32 v82, v86, v87
	v_lshlrev_b32_e32 v86, 16, v152
	v_cvt_pk_bf16_f32 v83, v88, v89
	v_cvt_pk_bf16_f32 v84, v84, v85
	v_cvt_pk_bf16_f32 v85, v90, v91
	s_cmp_eq_u32 s101, 1
	s_cbranch_scc1 .Lgs1_a_5
	global_store_dwordx4 v[196:197], v[82:85], off offset:256
	s_branch .Lgs1_b_5
.Lgs1_a_5:
	global_store_dwordx4 v[196:197], v[82:85], off offset:256 sc1
.Lgs1_b_5:
	v_and_b32_e32 v87, 0xffff0000, v152
	v_lshlrev_b32_e32 v88, 16, v153
	v_lshlrev_b32_e32 v82, 16, v150
	v_and_b32_e32 v83, 0xffff0000, v150
	v_lshlrev_b32_e32 v84, 16, v151
	v_and_b32_e32 v85, 0xffff0000, v151
	v_and_b32_e32 v89, 0xffff0000, v153
	v_pk_fma_f32 v[80:81], v[80:81], v[136:137], v[84:85]
	v_pk_fma_f32 v[78:79], v[78:79], v[134:135], v[82:83]
	v_pk_fma_f32 v[82:83], v[76:77], v[132:133], v[88:89]
	v_pk_fma_f32 v[76:77], v[74:75], v[130:131], v[86:87]
	v_cvt_pk_bf16_f32 v74, v78, v79
	v_cvt_pk_bf16_f32 v75, v80, v81
	v_lshlrev_b32_e32 v78, 16, v148
	v_cvt_pk_bf16_f32 v76, v76, v77
	v_cvt_pk_bf16_f32 v77, v82, v83
	s_cmp_eq_u32 s101, 1
	s_cbranch_scc1 .Lgs1_a_6
	global_store_dwordx4 v[194:195], v[74:77], off
	s_branch .Lgs1_b_6
.Lgs1_a_6:
	global_store_dwordx4 v[194:195], v[74:77], off sc1
.Lgs1_b_6:
	v_and_b32_e32 v79, 0xffff0000, v148
	v_lshlrev_b32_e32 v80, 16, v149
	v_lshlrev_b32_e32 v74, 16, v146
	v_and_b32_e32 v75, 0xffff0000, v146
	v_and_b32_e32 v81, 0xffff0000, v149
	v_lshlrev_b32_e32 v76, 16, v147
	v_and_b32_e32 v77, 0xffff0000, v147
	v_pk_fma_f32 v[70:71], v[70:71], v[126:127], v[74:75]
	v_pk_fma_f32 v[74:75], v[68:69], v[124:125], v[80:81]
	v_pk_fma_f32 v[68:69], v[66:67], v[122:123], v[78:79]
	v_pk_fma_f32 v[72:73], v[72:73], v[128:129], v[76:77]
	v_cvt_pk_bf16_f32 v66, v70, v71
	v_lshl_add_u64 v[102:103], v[192:193], 0, v[184:185]
	v_cvt_pk_bf16_f32 v67, v72, v73
	v_cvt_pk_bf16_f32 v68, v68, v69
	v_cvt_pk_bf16_f32 v69, v74, v75
	s_cmp_eq_u32 s101, 1
	s_cbranch_scc1 .Lgs1_a_7
	global_store_dwordx4 v[194:195], v[66:69], off offset:256
	s_branch .Lgs1_b_7
.Lgs1_a_7:
	global_store_dwordx4 v[194:195], v[66:69], off offset:256 sc1
.Lgs1_b_7:
	global_load_dwordx4 v[78:81], v[102:103], off
	global_load_dwordx4 v[82:85], v[102:103], off offset:256
	v_lshl_add_u64 v[104:105], v[192:193], 0, v[186:187]
	global_load_dwordx4 v[86:89], v[104:105], off
	global_load_dwordx4 v[90:93], v[104:105], off offset:256
	v_lshl_add_u64 v[76:77], v[192:193], 0, v[188:189]
	global_load_dwordx4 v[94:97], v[76:77], off
	global_load_dwordx4 v[98:101], v[76:77], off offset:256
	v_lshl_add_u64 v[74:75], v[192:193], 0, v[190:191]
	global_load_dwordx4 v[70:73], v[74:75], off
	global_load_dwordx4 v[66:69], v[74:75], off offset:256
	s_waitcnt vmcnt(0)
	v_lshlrev_b32_e32 v106, 16, v78
	v_and_b32_e32 v107, 0xffff0000, v78
	v_lshlrev_b32_e32 v78, 16, v79
	v_and_b32_e32 v79, 0xffff0000, v79
	v_lshlrev_b32_e32 v108, 16, v80
	v_and_b32_e32 v109, 0xffff0000, v80
	v_lshlrev_b32_e32 v80, 16, v81
	v_and_b32_e32 v81, 0xffff0000, v81
	v_pk_fma_f32 v[56:57], v[56:57], v[136:137], v[78:79]
	v_pk_fma_f32 v[54:55], v[54:55], v[134:135], v[106:107]
	v_pk_fma_f32 v[78:79], v[52:53], v[132:133], v[80:81]
	v_pk_fma_f32 v[52:53], v[50:51], v[130:131], v[108:109]
	v_cvt_pk_bf16_f32 v50, v54, v55
	v_cvt_pk_bf16_f32 v51, v56, v57
	v_lshlrev_b32_e32 v54, 16, v84
	v_cvt_pk_bf16_f32 v52, v52, v53
	v_cvt_pk_bf16_f32 v53, v78, v79
	s_cmp_eq_u32 s101, 1
	s_cbranch_scc1 .Lgs1_a_8
	global_store_dwordx4 v[102:103], v[50:53], off
	s_branch .Lgs1_b_8
.Lgs1_a_8:
	global_store_dwordx4 v[102:103], v[50:53], off sc1
.Lgs1_b_8:
	v_and_b32_e32 v55, 0xffff0000, v84
	v_lshlrev_b32_e32 v56, 16, v85
	v_lshlrev_b32_e32 v50, 16, v82
	v_and_b32_e32 v51, 0xffff0000, v82
	v_lshlrev_b32_e32 v52, 16, v83
	v_and_b32_e32 v53, 0xffff0000, v83
	v_and_b32_e32 v57, 0xffff0000, v85
	v_pk_fma_f32 v[50:51], v[62:63], v[126:127], v[50:51]
	v_pk_fma_f32 v[52:53], v[64:65], v[128:129], v[52:53]
	v_pk_fma_f32 v[56:57], v[60:61], v[124:125], v[56:57]
	v_pk_fma_f32 v[54:55], v[58:59], v[122:123], v[54:55]
	v_cvt_pk_bf16_f32 v50, v50, v51
	v_cvt_pk_bf16_f32 v51, v52, v53
	s_nop 0
	v_cvt_pk_bf16_f32 v52, v54, v55
	v_cvt_pk_bf16_f32 v53, v56, v57
	s_cmp_eq_u32 s101, 1
	s_cbranch_scc1 .Lgs1_a_9
	global_store_dwordx4 v[102:103], v[50:53], off offset:256
	s_branch .Lgs1_b_9
.Lgs1_a_9:
	global_store_dwordx4 v[102:103], v[50:53], off offset:256 sc1
.Lgs1_b_9:
	v_lshlrev_b32_e32 v54, 16, v88
	v_and_b32_e32 v55, 0xffff0000, v88
	v_lshlrev_b32_e32 v50, 16, v86
	v_and_b32_e32 v51, 0xffff0000, v86
	v_lshlrev_b32_e32 v56, 16, v89
	v_and_b32_e32 v57, 0xffff0000, v89
	v_lshlrev_b32_e32 v52, 16, v87
	v_and_b32_e32 v53, 0xffff0000, v87
	v_pk_fma_f32 v[38:39], v[38:39], v[134:135], v[50:51]
	v_pk_fma_f32 v[50:51], v[36:37], v[132:133], v[56:57]
	v_pk_fma_f32 v[36:37], v[34:35], v[130:131], v[54:55]
	v_pk_fma_f32 v[40:41], v[40:41], v[136:137], v[52:53]
	v_cvt_pk_bf16_f32 v34, v38, v39
	v_lshlrev_b32_e32 v38, 16, v92
	v_cvt_pk_bf16_f32 v35, v40, v41
	v_cvt_pk_bf16_f32 v36, v36, v37
	v_cvt_pk_bf16_f32 v37, v50, v51
	s_cmp_eq_u32 s101, 1
	s_cbranch_scc1 .Lgs1_a_10
	global_store_dwordx4 v[104:105], v[34:37], off
	s_branch .Lgs1_b_10
.Lgs1_a_10:
	global_store_dwordx4 v[104:105], v[34:37], off sc1
.Lgs1_b_10:
	v_and_b32_e32 v39, 0xffff0000, v92
	v_lshlrev_b32_e32 v40, 16, v93
	v_lshlrev_b32_e32 v34, 16, v90
	v_and_b32_e32 v35, 0xffff0000, v90
	v_lshlrev_b32_e32 v36, 16, v91
	v_and_b32_e32 v37, 0xffff0000, v91
	v_and_b32_e32 v41, 0xffff0000, v93
	v_pk_fma_f32 v[36:37], v[48:49], v[128:129], v[36:37]
	v_pk_fma_f32 v[34:35], v[46:47], v[126:127], v[34:35]
	v_pk_fma_f32 v[40:41], v[44:45], v[124:125], v[40:41]
	v_pk_fma_f32 v[38:39], v[42:43], v[122:123], v[38:39]
	v_cvt_pk_bf16_f32 v34, v34, v35
	v_cvt_pk_bf16_f32 v35, v36, v37
	s_nop 0
	v_cvt_pk_bf16_f32 v36, v38, v39
	v_cvt_pk_bf16_f32 v37, v40, v41
	s_cmp_eq_u32 s101, 1
	s_cbranch_scc1 .Lgs1_a_11
	global_store_dwordx4 v[104:105], v[34:37], off offset:256
	s_branch .Lgs1_b_11
.Lgs1_a_11:
	global_store_dwordx4 v[104:105], v[34:37], off offset:256 sc1
.Lgs1_b_11:
	v_lshlrev_b32_e32 v38, 16, v96
	v_and_b32_e32 v39, 0xffff0000, v96
	v_lshlrev_b32_e32 v34, 16, v94
	v_and_b32_e32 v35, 0xffff0000, v94
	v_lshlrev_b32_e32 v36, 16, v95
	v_and_b32_e32 v37, 0xffff0000, v95
	v_lshlrev_b32_e32 v40, 16, v97
	v_and_b32_e32 v41, 0xffff0000, v97
	v_pk_fma_f32 v[24:25], v[24:25], v[136:137], v[36:37]
	v_pk_fma_f32 v[22:23], v[22:23], v[134:135], v[34:35]
	v_pk_fma_f32 v[34:35], v[20:21], v[132:133], v[40:41]
	v_pk_fma_f32 v[20:21], v[18:19], v[130:131], v[38:39]
	v_cvt_pk_bf16_f32 v18, v22, v23
	v_cvt_pk_bf16_f32 v19, v24, v25
	v_lshlrev_b32_e32 v22, 16, v100
	v_cvt_pk_bf16_f32 v20, v20, v21
	v_cvt_pk_bf16_f32 v21, v34, v35
	s_cmp_eq_u32 s101, 1
	s_cbranch_scc1 .Lgs1_a_12
	global_store_dwordx4 v[76:77], v[18:21], off
	s_branch .Lgs1_b_12
.Lgs1_a_12:
	global_store_dwordx4 v[76:77], v[18:21], off sc1
.Lgs1_b_12:
	v_and_b32_e32 v23, 0xffff0000, v100
	v_lshlrev_b32_e32 v24, 16, v101
	v_lshlrev_b32_e32 v18, 16, v98
	v_and_b32_e32 v19, 0xffff0000, v98
	v_lshlrev_b32_e32 v20, 16, v99
	v_and_b32_e32 v21, 0xffff0000, v99
	v_and_b32_e32 v25, 0xffff0000, v101
	v_pk_fma_f32 v[18:19], v[30:31], v[126:127], v[18:19]
	v_pk_fma_f32 v[20:21], v[32:33], v[128:129], v[20:21]
	v_pk_fma_f32 v[24:25], v[28:29], v[124:125], v[24:25]
	v_pk_fma_f32 v[22:23], v[26:27], v[122:123], v[22:23]
	v_cvt_pk_bf16_f32 v18, v18, v19
	v_cvt_pk_bf16_f32 v19, v20, v21
	s_nop 0
	v_cvt_pk_bf16_f32 v20, v22, v23
	v_cvt_pk_bf16_f32 v21, v24, v25
	s_cmp_eq_u32 s101, 1
	s_cbranch_scc1 .Lgs1_a_13
	global_store_dwordx4 v[76:77], v[18:21], off offset:256
	s_branch .Lgs1_b_13
.Lgs1_a_13:
	global_store_dwordx4 v[76:77], v[18:21], off offset:256 sc1
.Lgs1_b_13:
	v_lshlrev_b32_e32 v22, 16, v72
	v_and_b32_e32 v23, 0xffff0000, v72
	v_lshlrev_b32_e32 v18, 16, v70
	v_and_b32_e32 v19, 0xffff0000, v70
	v_lshlrev_b32_e32 v24, 16, v73
	v_and_b32_e32 v25, 0xffff0000, v73
	v_lshlrev_b32_e32 v20, 16, v71
	v_and_b32_e32 v21, 0xffff0000, v71
	v_pk_fma_f32 v[6:7], v[6:7], v[134:135], v[18:19]
	v_pk_fma_f32 v[18:19], v[4:5], v[132:133], v[24:25]
	v_pk_fma_f32 v[4:5], v[2:3], v[130:131], v[22:23]
	v_pk_fma_f32 v[8:9], v[8:9], v[136:137], v[20:21]
	v_cvt_pk_bf16_f32 v2, v6, v7
	v_lshlrev_b32_e32 v6, 16, v68
	v_cvt_pk_bf16_f32 v3, v8, v9
	v_cvt_pk_bf16_f32 v4, v4, v5
	v_cvt_pk_bf16_f32 v5, v18, v19
	s_cmp_eq_u32 s101, 1
	s_cbranch_scc1 .Lgs1_a_14
	global_store_dwordx4 v[74:75], v[2:5], off
	s_branch .Lgs1_b_14
.Lgs1_a_14:
	global_store_dwordx4 v[74:75], v[2:5], off sc1
.Lgs1_b_14:
	v_and_b32_e32 v7, 0xffff0000, v68
	v_lshlrev_b32_e32 v8, 16, v69
	v_lshlrev_b32_e32 v2, 16, v66
	v_and_b32_e32 v3, 0xffff0000, v66
	v_lshlrev_b32_e32 v4, 16, v67
	v_and_b32_e32 v5, 0xffff0000, v67
	v_and_b32_e32 v9, 0xffff0000, v69
	v_pk_fma_f32 v[4:5], v[16:17], v[128:129], v[4:5]
	v_pk_fma_f32 v[2:3], v[14:15], v[126:127], v[2:3]
	v_pk_fma_f32 v[8:9], v[12:13], v[124:125], v[8:9]
	v_pk_fma_f32 v[6:7], v[10:11], v[122:123], v[6:7]
	v_mov_b32_e32 v126, v207
	v_mov_b32_e32 v128, v206
	v_mov_b32_e32 v124, v205
	v_mov_b32_e32 v122, v204
	v_cvt_pk_bf16_f32 v2, v2, v3
	v_cvt_pk_bf16_f32 v3, v4, v5
	v_cvt_pk_bf16_f32 v4, v6, v7
	v_cvt_pk_bf16_f32 v5, v8, v9
	s_cmp_eq_u32 s101, 1
	s_cbranch_scc1 .Lgs1_a_15
	global_store_dwordx4 v[74:75], v[2:5], off offset:256
	s_branch .Lgs1_b_15
.Lgs1_a_15:
	global_store_dwordx4 v[74:75], v[2:5], off offset:256 sc1
.Lgs1_b_15:
	s_cbranch_vccnz .LBB0_992
.LBB0_986:
	s_add_i32 s45, s45, 1
	s_mul_i32 s4, s45, s44
	s_mul_hi_u32 s5, s45, s79
	s_add_i32 s5, s5, s4
	s_mul_i32 s4, s45, s79
	s_add_u32 s18, s4, s26
	s_addc_u32 s19, s5, s34
	s_cmp_ge_u32 s18, s12
	s_cselect_b32 s101, 1, 0
	v_mov_b64_e32 v[2:3], s[12:13]
	v_cmp_ge_i64_e64 s[4:5], s[18:19], v[2:3]
	v_cmp_lt_i64_e64 s[6:7], s[18:19], v[2:3]
	s_and_b64 vcc, exec, s[4:5]
	s_cbranch_vccnz .LBB0_988
	s_ashr_i32 s16, s18, 31
	s_lshr_b32 s16, s16, 29
	s_add_i32 s16, s18, s16
	s_ashr_i32 s17, s16, 3
	s_and_b32 s16, s16, -8
	s_sub_i32 s16, s18, s16
	s_cmp_lt_i32 s16, 0
	s_cselect_b32 s18, s35, s31
	s_mul_i32 s16, s18, s16
	s_add_i32 s16, s16, s17
	s_ashr_i32 s17, s16, 31
	s_lshr_b32 s17, s17, 27
	s_add_i32 s17, s16, s17
	s_ashr_i32 s18, s17, 5
	s_lshl_b32 s18, s18, 3
	s_sub_i32 s19, s25, s18
	s_min_i32 s19, s19, 8
	s_abs_i32 s20, s19
	v_cvt_f32_u32_e32 v2, s20
	s_sub_i32 s22, 0, s20
	s_andn2_b32 s17, s17, 31
	s_sub_i32 s17, s16, s17
	v_rcp_iflag_f32_e32 v2, v2
	s_abs_i32 s16, s17
	s_xor_b32 s21, s17, s19
	s_ashr_i32 s21, s21, 31
	v_mul_f32_e32 v2, 0x4f7ffffe, v2
	v_cvt_u32_f32_e32 v2, v2
	s_nop 0
	v_readfirstlane_b32 s23, v2
	s_mul_i32 s22, s22, s23
	s_mul_hi_u32 s22, s23, s22
	s_add_i32 s23, s23, s22
	s_mul_hi_u32 s22, s16, s23
	s_mul_i32 s23, s22, s20
	s_sub_i32 s16, s16, s23
	s_add_i32 s33, s22, 1
	s_sub_i32 s23, s16, s20
	s_cmp_ge_u32 s16, s20
	s_cselect_b32 s22, s33, s22
	s_cselect_b32 s16, s23, s16
	s_add_i32 s23, s22, 1
	s_cmp_ge_u32 s16, s20
	s_cselect_b32 s16, s23, s22
	s_xor_b32 s16, s16, s21
	s_sub_i32 s16, s16, s21
	s_mul_i32 s19, s16, s19
	s_sub_i32 s17, s17, s19
	s_add_i32 s46, s17, s18

.LBB0_1233:
	s_add_i32 s40, s40, 1
	s_mul_i32 s4, s40, s39
	s_mul_hi_u32 s5, s40, s79
	s_add_i32 s5, s5, s4
	s_mul_i32 s4, s40, s79
	s_add_u32 s6, s4, s26
	s_addc_u32 s7, s5, s29
	s_cmp_ge_u32 s6, s18
	s_cselect_b32 s101, 1, 0
	v_mov_b64_e32 v[2:3], s[18:19]
	v_cmp_ge_i64_e64 s[4:5], s[6:7], v[2:3]
	v_cmp_lt_i64_e64 s[8:9], s[6:7], v[2:3]
	s_and_b64 vcc, exec, s[4:5]
	s_cbranch_vccnz .LBB0_1235
	s_ashr_i32 s7, s6, 31
	s_lshr_b32 s7, s7, 29
	s_add_i32 s7, s6, s7
	s_ashr_i32 s22, s7, 3
	s_and_b32 s7, s7, -8
	s_sub_i32 s6, s6, s7
	s_lshr_b32 s7, s6, 31
	s_or_b32 s7, s7, s28
	s_mul_i32 s6, s7, s6
	s_add_i32 s6, s6, s22
	s_ashr_i32 s7, s6, 31
	s_lshr_b32 s7, s7, 26
	s_add_i32 s7, s6, s7
	s_ashr_i32 s22, s7, 6
	s_lshl_b32 s23, s22, 3
	s_sub_i32 s22, s28, s23
	s_min_i32 s24, s22, 8
	s_abs_i32 s22, s24
	v_cvt_f32_u32_e32 v2, s22
	s_sub_i32 s33, 0, s22
	s_andn2_b32 s7, s7, 63
	s_sub_i32 s6, s6, s7
	v_rcp_iflag_f32_e32 v2, v2
	s_abs_i32 s7, s6
	s_xor_b32 s25, s6, s24
	s_ashr_i32 s25, s25, 31
	v_mul_f32_e32 v2, 0x4f7ffffe, v2
	v_cvt_u32_f32_e32 v2, v2
	s_nop 0
	v_readfirstlane_b32 s41, v2
	s_mul_i32 s33, s33, s41
	s_mul_hi_u32 s33, s41, s33
	s_add_i32 s41, s41, s33
	s_mul_hi_u32 s33, s7, s41
	s_mul_i32 s41, s33, s22
	s_sub_i32 s7, s7, s41
	s_add_i32 s44, s33, 1
	s_sub_i32 s41, s7, s22
	s_cmp_ge_u32 s7, s22
	s_cselect_b32 s33, s44, s33
	s_cselect_b32 s7, s41, s7
	s_add_i32 s41, s33, 1
	s_cmp_ge_u32 s7, s22
	s_cselect_b32 s7, s41, s33
	s_xor_b32 s7, s7, s25
	s_sub_i32 s22, s7, s25
	s_mul_i32 s7, s22, s24
	s_sub_i32 s6, s6, s7
	s_add_i32 s41, s6, s23

.LBB0_1246:
	s_add_u32 s6, s10, s0
	s_addc_u32 s7, s11, s1
	s_add_u32 s24, s6, 0x100
	s_addc_u32 s25, s7, 0
	s_add_u32 s33, s23, s0
	s_addc_u32 s46, s44, s1
	s_cmpk_eq_i32 s0, 0x700
	s_cselect_b64 vcc, -1, 0
	s_and_b64 s[6:7], vcc, exec
	s_cselect_b32 s25, s11, s25
	s_cselect_b32 s24, s10, s24
	s_cselect_b32 s7, s9, s46
	s_cselect_b32 s6, s8, s33
	s_add_i32 s33, 0, 0x10000
	v_add_u32_e32 v165, s33, v141
	ds_read_b128 v[156:159], v165
	ds_read_b128 v[160:163], v165 offset:1024
	ds_read_b128 v[172:175], v165 offset:2048
	ds_read_b128 v[176:179], v165 offset:3072
	v_cndmask_b32_e32 v226, v140, v152, vcc
	v_cndmask_b32_e32 v164, v138, v153, vcc
	v_cndmask_b32_e32 v135, v136, v154, vcc
	v_cndmask_b32_e32 v137, v134, v155, vcc
	v_lshl_add_u64 v[166:167], v[144:145], 0, s[0:1]
	s_add_i32 m0, s31, 0xc000
	ds_read_b128 v[180:183], v151
	ds_read_b128 v[184:187], v151 offset:1024
	ds_read_b128 v[188:191], v151 offset:2048
	ds_read_b128 v[192:195], v151 offset:3072
	ds_read_b128 v[196:199], v151 offset:4096
	ds_read_b128 v[200:203], v151 offset:5120
	ds_read_b128 v[204:207], v151 offset:6144
	ds_read_b128 v[208:211], v151 offset:7168
	global_load_lds_dwordx4 v[166:167], off
	v_lshl_add_u64 v[166:167], v[142:143], 0, s[0:1]
	s_add_i32 m0, s31, 0xe000
	s_nop 0
	global_load_lds_dwordx4 v[166:167], off
	s_waitcnt lgkmcnt(8)
	s_barrier
	s_waitcnt lgkmcnt(0)
	s_setprio 1
	s_waitcnt lgkmcnt(0)
	v_mfma_f32_16x16x32_bf16 v[126:129], v[156:159], v[180:183], v[126:129]
	v_mfma_f32_16x16x32_bf16 v[118:121], v[172:175], v[180:183], v[118:121]
	v_mfma_f32_16x16x32_bf16 v[110:113], v[156:159], v[188:191], v[110:113]
	v_mfma_f32_16x16x32_bf16 v[102:105], v[172:175], v[188:191], v[102:105]
	v_mfma_f32_16x16x32_bf16 v[94:97], v[156:159], v[196:199], v[94:97]
	v_mfma_f32_16x16x32_bf16 v[86:89], v[172:175], v[196:199], v[86:89]
	v_mfma_f32_16x16x32_bf16 v[78:81], v[156:159], v[204:207], v[78:81]
	v_mfma_f32_16x16x32_bf16 v[70:73], v[172:175], v[204:207], v[70:73]
	v_mfma_f32_16x16x32_bf16 v[126:129], v[160:163], v[184:187], v[126:129]
	v_mfma_f32_16x16x32_bf16 v[118:121], v[176:179], v[184:187], v[118:121]
	v_mfma_f32_16x16x32_bf16 v[110:113], v[160:163], v[192:195], v[110:113]
	v_mfma_f32_16x16x32_bf16 v[102:105], v[176:179], v[192:195], v[102:105]
	v_mfma_f32_16x16x32_bf16 v[94:97], v[160:163], v[200:203], v[94:97]
	v_mfma_f32_16x16x32_bf16 v[86:89], v[176:179], v[200:203], v[86:89]
	v_mfma_f32_16x16x32_bf16 v[78:81], v[160:163], v[208:211], v[78:81]
	v_mfma_f32_16x16x32_bf16 v[70:73], v[176:179], v[208:211], v[70:73]
	s_setprio 0
	s_barrier
	s_add_i32 s48, 0, 0x14000
	s_add_i32 s33, s33, s30
	v_add_u32_e32 v165, s48, v141
	v_lshl_add_u64 v[166:167], s[6:7], 0, v[130:131]
	s_mov_b32 m0, s33
	ds_read_b128 v[212:215], v165
	ds_read_b128 v[230:233], v165 offset:1024
	ds_read_b128 v[234:237], v165 offset:2048
	ds_read_b128 v[238:241], v165 offset:3072
	global_load_lds_dwordx4 v[166:167], off
	v_lshl_add_u64 v[220:221], s[6:7], 0, v[132:133]
	s_add_i32 m0, s33, 0x2000
	s_nop 0
	global_load_lds_dwordx4 v[220:221], off
	s_barrier
	s_waitcnt lgkmcnt(0)
	s_setprio 1
	s_waitcnt lgkmcnt(0)
	v_mfma_f32_16x16x32_bf16 v[122:125], v[212:215], v[180:183], v[122:125]
	v_mfma_f32_16x16x32_bf16 v[114:117], v[234:237], v[180:183], v[114:117]
	v_mfma_f32_16x16x32_bf16 v[106:109], v[212:215], v[188:191], v[106:109]
	v_mfma_f32_16x16x32_bf16 v[98:101], v[234:237], v[188:191], v[98:101]
	v_mfma_f32_16x16x32_bf16 v[90:93], v[212:215], v[196:199], v[90:93]
	v_mfma_f32_16x16x32_bf16 v[82:85], v[234:237], v[196:199], v[82:85]
	v_mfma_f32_16x16x32_bf16 v[74:77], v[212:215], v[204:207], v[74:77]
	v_mfma_f32_16x16x32_bf16 v[66:69], v[234:237], v[204:207], v[66:69]
	v_mfma_f32_16x16x32_bf16 v[122:125], v[230:233], v[184:187], v[122:125]
	v_mfma_f32_16x16x32_bf16 v[114:117], v[238:241], v[184:187], v[114:117]
	v_mfma_f32_16x16x32_bf16 v[106:109], v[230:233], v[192:195], v[106:109]
	v_mfma_f32_16x16x32_bf16 v[98:101], v[238:241], v[192:195], v[98:101]
	v_mfma_f32_16x16x32_bf16 v[90:93], v[230:233], v[200:203], v[90:93]
	v_mfma_f32_16x16x32_bf16 v[82:85], v[238:241], v[200:203], v[82:85]
	v_mfma_f32_16x16x32_bf16 v[74:77], v[230:233], v[208:211], v[74:77]
	v_mfma_f32_16x16x32_bf16 v[66:69], v[238:241], v[208:211], v[66:69]
	s_setprio 0
	s_mov_b32 m0, s31
	s_barrier
	ds_read_b128 v[180:183], v151 offset:16384
	ds_read_b128 v[184:187], v151 offset:17408
	ds_read_b128 v[188:191], v151 offset:18432
	ds_read_b128 v[192:195], v151 offset:19456
	ds_read_b128 v[196:199], v151 offset:20480
	ds_read_b128 v[200:203], v151 offset:21504
	ds_read_b128 v[204:207], v151 offset:22528
	ds_read_b128 v[208:211], v151 offset:23552
	global_load_lds_dwordx4 v226, s[24:25]
	s_mov_b32 m0, s34
	v_mov_b32_e32 v165, v227
	global_load_lds_dwordx4 v164, s[24:25]
	s_barrier
	s_waitcnt lgkmcnt(0)
	v_lshl_add_u64 v[222:223], s[24:25], 0, v[226:227]
	v_lshl_add_u64 v[164:165], s[24:25], 0, v[164:165]
	s_setprio 1
	s_waitcnt lgkmcnt(0)
	v_mfma_f32_16x16x32_bf16 v[58:61], v[156:159], v[180:183], v[58:61]
	v_mfma_f32_16x16x32_bf16 v[50:53], v[172:175], v[180:183], v[50:53]
	v_mfma_f32_16x16x32_bf16 v[42:45], v[156:159], v[188:191], v[42:45]
	v_mfma_f32_16x16x32_bf16 v[34:37], v[172:175], v[188:191], v[34:37]
	v_mfma_f32_16x16x32_bf16 v[26:29], v[156:159], v[196:199], v[26:29]
	v_mfma_f32_16x16x32_bf16 v[18:21], v[172:175], v[196:199], v[18:21]
	v_mfma_f32_16x16x32_bf16 v[6:9], v[156:159], v[204:207], v[6:9]
	v_mfma_f32_16x16x32_bf16 v[2:5], v[172:175], v[204:207], v[2:5]
	v_mfma_f32_16x16x32_bf16 v[58:61], v[160:163], v[184:187], v[58:61]
	v_mfma_f32_16x16x32_bf16 v[50:53], v[176:179], v[184:187], v[50:53]
	v_mfma_f32_16x16x32_bf16 v[42:45], v[160:163], v[192:195], v[42:45]
	v_mfma_f32_16x16x32_bf16 v[34:37], v[176:179], v[192:195], v[34:37]
	v_mfma_f32_16x16x32_bf16 v[26:29], v[160:163], v[200:203], v[26:29]
	v_mfma_f32_16x16x32_bf16 v[18:21], v[176:179], v[200:203], v[18:21]
	v_mfma_f32_16x16x32_bf16 v[6:9], v[160:163], v[208:211], v[6:9]
	v_mfma_f32_16x16x32_bf16 v[2:5], v[176:179], v[208:211], v[2:5]
	s_setprio 0
	s_barrier
	s_add_u32 s46, s6, 0x40000
	s_addc_u32 s47, s7, 0
	s_add_i32 s33, s48, s30
	v_lshl_add_u64 v[156:157], s[46:47], 0, v[130:131]
	s_mov_b32 m0, s33
	s_nop 0
	global_load_lds_dwordx4 v[156:157], off
	v_lshl_add_u64 v[156:157], s[46:47], 0, v[132:133]
	s_add_i32 m0, s33, 0x2000
	s_nop 0
	global_load_lds_dwordx4 v[156:157], off
	s_waitcnt vmcnt(6)
	s_barrier
	s_setprio 1
	v_mfma_f32_16x16x32_bf16 v[62:65], v[212:215], v[180:183], v[62:65]
	v_mfma_f32_16x16x32_bf16 v[54:57], v[234:237], v[180:183], v[54:57]
	v_mfma_f32_16x16x32_bf16 v[46:49], v[212:215], v[188:191], v[46:49]
	v_mfma_f32_16x16x32_bf16 v[38:41], v[234:237], v[188:191], v[38:41]
	v_mfma_f32_16x16x32_bf16 v[30:33], v[212:215], v[196:199], v[30:33]
	v_mfma_f32_16x16x32_bf16 v[22:25], v[234:237], v[196:199], v[22:25]
	v_mfma_f32_16x16x32_bf16 v[14:17], v[212:215], v[204:207], v[14:17]
	v_mfma_f32_16x16x32_bf16 v[10:13], v[234:237], v[204:207], v[10:13]
	v_mfma_f32_16x16x32_bf16 v[62:65], v[230:233], v[184:187], v[62:65]
	v_mfma_f32_16x16x32_bf16 v[54:57], v[238:241], v[184:187], v[54:57]
	v_mfma_f32_16x16x32_bf16 v[46:49], v[230:233], v[192:195], v[46:49]
	v_mfma_f32_16x16x32_bf16 v[38:41], v[238:241], v[192:195], v[38:41]
	v_mfma_f32_16x16x32_bf16 v[30:33], v[230:233], v[200:203], v[30:33]
	v_mfma_f32_16x16x32_bf16 v[22:25], v[238:241], v[200:203], v[22:25]
	v_mfma_f32_16x16x32_bf16 v[14:17], v[230:233], v[208:211], v[14:17]
	v_mfma_f32_16x16x32_bf16 v[10:13], v[238:241], v[208:211], v[10:13]
	s_setprio 0
	s_add_i32 s33, 0, 0x18000
	v_add_u32_e32 v171, s33, v141
	s_barrier
	ds_read_b128 v[156:159], v171
	ds_read_b128 v[160:163], v171 offset:1024
	ds_read_b128 v[172:175], v171 offset:2048
	ds_read_b128 v[176:179], v171 offset:3072
	s_mov_b32 m0, s35
	ds_read_b128 v[180:183], v151 offset:32768
	ds_read_b128 v[184:187], v151 offset:33792
	ds_read_b128 v[188:191], v151 offset:34816
	ds_read_b128 v[192:195], v151 offset:35840
	ds_read_b128 v[196:199], v151 offset:36864
	ds_read_b128 v[200:203], v151 offset:37888
	ds_read_b128 v[204:207], v151 offset:38912
	ds_read_b128 v[208:211], v151 offset:39936
	global_load_lds_dwordx4 v135, s[24:25]
	s_mov_b32 m0, s36
	s_nop 0
	global_load_lds_dwordx4 v137, s[24:25]
	s_waitcnt lgkmcnt(8)
	s_barrier
	s_waitcnt lgkmcnt(0)
	s_setprio 1
	s_waitcnt lgkmcnt(0)
	v_mfma_f32_16x16x32_bf16 v[126:129], v[156:159], v[180:183], v[126:129]
	v_mfma_f32_16x16x32_bf16 v[118:121], v[172:175], v[180:183], v[118:121]
	v_mfma_f32_16x16x32_bf16 v[110:113], v[156:159], v[188:191], v[110:113]
	v_mfma_f32_16x16x32_bf16 v[102:105], v[172:175], v[188:191], v[102:105]
	v_mfma_f32_16x16x32_bf16 v[94:97], v[156:159], v[196:199], v[94:97]
	v_mfma_f32_16x16x32_bf16 v[86:89], v[172:175], v[196:199], v[86:89]
	v_mfma_f32_16x16x32_bf16 v[78:81], v[156:159], v[204:207], v[78:81]
	v_mfma_f32_16x16x32_bf16 v[70:73], v[172:175], v[204:207], v[70:73]
	v_mfma_f32_16x16x32_bf16 v[126:129], v[160:163], v[184:187], v[126:129]
	v_mfma_f32_16x16x32_bf16 v[118:121], v[176:179], v[184:187], v[118:121]
	v_mfma_f32_16x16x32_bf16 v[110:113], v[160:163], v[192:195], v[110:113]
	v_mfma_f32_16x16x32_bf16 v[102:105], v[176:179], v[192:195], v[102:105]
	v_mfma_f32_16x16x32_bf16 v[94:97], v[160:163], v[200:203], v[94:97]
	v_mfma_f32_16x16x32_bf16 v[86:89], v[176:179], v[200:203], v[86:89]
	v_mfma_f32_16x16x32_bf16 v[78:81], v[160:163], v[208:211], v[78:81]
	v_mfma_f32_16x16x32_bf16 v[70:73], v[176:179], v[208:211], v[70:73]
	s_setprio 0
	s_barrier
	s_add_i32 s24, 0, 0x1c000
	s_add_i32 s25, s33, s30
	v_add_u32_e32 v135, s24, v141
	v_lshl_add_u64 v[166:167], v[166:167], 0, s[96:97]
	s_mov_b32 m0, s25
	ds_read_b128 v[212:215], v135
	ds_read_b128 v[230:233], v135 offset:1024
	ds_read_b128 v[234:237], v135 offset:2048
	ds_read_b128 v[238:241], v135 offset:3072
	global_load_lds_dwordx4 v[166:167], off
	v_lshl_add_u64 v[166:167], v[220:221], 0, s[96:97]
	s_add_i32 m0, s25, 0x2000
	s_nop 0
	global_load_lds_dwordx4 v[166:167], off
	s_barrier
	s_waitcnt lgkmcnt(0)
	s_setprio 1
	s_waitcnt lgkmcnt(0)
	v_mfma_f32_16x16x32_bf16 v[122:125], v[212:215], v[180:183], v[122:125]
	v_mfma_f32_16x16x32_bf16 v[114:117], v[234:237], v[180:183], v[114:117]
	v_mfma_f32_16x16x32_bf16 v[106:109], v[212:215], v[188:191], v[106:109]
	v_mfma_f32_16x16x32_bf16 v[98:101], v[234:237], v[188:191], v[98:101]
	v_mfma_f32_16x16x32_bf16 v[90:93], v[212:215], v[196:199], v[90:93]
	v_mfma_f32_16x16x32_bf16 v[82:85], v[234:237], v[196:199], v[82:85]
	v_mfma_f32_16x16x32_bf16 v[74:77], v[212:215], v[204:207], v[74:77]
	v_mfma_f32_16x16x32_bf16 v[66:69], v[234:237], v[204:207], v[66:69]
	v_mfma_f32_16x16x32_bf16 v[122:125], v[230:233], v[184:187], v[122:125]
	v_mfma_f32_16x16x32_bf16 v[114:117], v[238:241], v[184:187], v[114:117]
	v_mfma_f32_16x16x32_bf16 v[106:109], v[230:233], v[192:195], v[106:109]
	v_mfma_f32_16x16x32_bf16 v[98:101], v[238:241], v[192:195], v[98:101]
	v_mfma_f32_16x16x32_bf16 v[90:93], v[230:233], v[200:203], v[90:93]
	v_mfma_f32_16x16x32_bf16 v[82:85], v[238:241], v[200:203], v[82:85]
	v_mfma_f32_16x16x32_bf16 v[74:77], v[230:233], v[208:211], v[74:77]
	v_mfma_f32_16x16x32_bf16 v[66:69], v[238:241], v[208:211], v[66:69]
	s_setprio 0
	s_mov_b32 m0, s37
	v_lshl_add_u64 v[166:167], v[222:223], 0, s[96:97]
	s_barrier
	ds_read_b128 v[180:183], v151 offset:49152
	ds_read_b128 v[184:187], v151 offset:50176
	ds_read_b128 v[188:191], v151 offset:51200
	ds_read_b128 v[192:195], v151 offset:52224
	ds_read_b128 v[196:199], v151 offset:53248
	ds_read_b128 v[200:203], v151 offset:54272
	ds_read_b128 v[204:207], v151 offset:55296
	ds_read_b128 v[208:211], v151 offset:56320
	global_load_lds_dwordx4 v[166:167], off
	v_lshl_add_u64 v[164:165], v[164:165], 0, s[96:97]
	s_mov_b32 m0, s38
	s_nop 0
	global_load_lds_dwordx4 v[164:165], off
	s_barrier
	s_waitcnt lgkmcnt(0)
	s_setprio 1
	s_waitcnt lgkmcnt(0)
	v_mfma_f32_16x16x32_bf16 v[58:61], v[156:159], v[180:183], v[58:61]
	v_mfma_f32_16x16x32_bf16 v[50:53], v[172:175], v[180:183], v[50:53]
	v_mfma_f32_16x16x32_bf16 v[42:45], v[156:159], v[188:191], v[42:45]
	v_mfma_f32_16x16x32_bf16 v[34:37], v[172:175], v[188:191], v[34:37]
	v_mfma_f32_16x16x32_bf16 v[26:29], v[156:159], v[196:199], v[26:29]
	v_mfma_f32_16x16x32_bf16 v[18:21], v[172:175], v[196:199], v[18:21]
	v_mfma_f32_16x16x32_bf16 v[6:9], v[156:159], v[204:207], v[6:9]
	v_mfma_f32_16x16x32_bf16 v[2:5], v[172:175], v[204:207], v[2:5]
	v_mfma_f32_16x16x32_bf16 v[58:61], v[160:163], v[184:187], v[58:61]
	v_mfma_f32_16x16x32_bf16 v[50:53], v[176:179], v[184:187], v[50:53]
	v_mfma_f32_16x16x32_bf16 v[42:45], v[160:163], v[192:195], v[42:45]
	v_mfma_f32_16x16x32_bf16 v[34:37], v[176:179], v[192:195], v[34:37]
	v_mfma_f32_16x16x32_bf16 v[26:29], v[160:163], v[200:203], v[26:29]
	v_mfma_f32_16x16x32_bf16 v[18:21], v[176:179], v[200:203], v[18:21]
	v_mfma_f32_16x16x32_bf16 v[6:9], v[160:163], v[208:211], v[6:9]
	v_mfma_f32_16x16x32_bf16 v[2:5], v[176:179], v[208:211], v[2:5]
	s_setprio 0
	s_barrier
	s_add_u32 s6, s6, 0x40080
	s_addc_u32 s7, s7, 0
	s_add_i32 s24, s24, s30
	v_lshl_add_u64 v[156:157], s[6:7], 0, v[130:131]
	s_mov_b32 m0, s24
	s_nop 0
	global_load_lds_dwordx4 v[156:157], off
	v_lshl_add_u64 v[156:157], s[6:7], 0, v[132:133]
	s_add_i32 m0, s24, 0x2000
	s_nop 0
	global_load_lds_dwordx4 v[156:157], off
	s_waitcnt vmcnt(6)
	s_barrier
	s_setprio 1
	v_mfma_f32_16x16x32_bf16 v[62:65], v[212:215], v[180:183], v[62:65]
	v_mfma_f32_16x16x32_bf16 v[54:57], v[234:237], v[180:183], v[54:57]
	v_mfma_f32_16x16x32_bf16 v[46:49], v[212:215], v[188:191], v[46:49]
	v_mfma_f32_16x16x32_bf16 v[38:41], v[234:237], v[188:191], v[38:41]
	v_mfma_f32_16x16x32_bf16 v[30:33], v[212:215], v[196:199], v[30:33]
	v_mfma_f32_16x16x32_bf16 v[22:25], v[234:237], v[196:199], v[22:25]
	v_mfma_f32_16x16x32_bf16 v[14:17], v[212:215], v[204:207], v[14:17]
	v_mfma_f32_16x16x32_bf16 v[10:13], v[234:237], v[204:207], v[10:13]
	v_mfma_f32_16x16x32_bf16 v[62:65], v[230:233], v[184:187], v[62:65]
	v_mfma_f32_16x16x32_bf16 v[54:57], v[238:241], v[184:187], v[54:57]
	v_mfma_f32_16x16x32_bf16 v[46:49], v[230:233], v[192:195], v[46:49]
	v_mfma_f32_16x16x32_bf16 v[38:41], v[238:241], v[192:195], v[38:41]
	v_mfma_f32_16x16x32_bf16 v[30:33], v[230:233], v[200:203], v[30:33]
	v_mfma_f32_16x16x32_bf16 v[22:25], v[238:241], v[200:203], v[22:25]
	v_mfma_f32_16x16x32_bf16 v[14:17], v[230:233], v[208:211], v[14:17]
	v_mfma_f32_16x16x32_bf16 v[10:13], v[238:241], v[208:211], v[10:13]
	s_setprio 0
	s_add_i32 s45, s45, 2
	s_add_u32 s0, s0, 0x100
	s_addc_u32 s1, s1, 0
	s_cmp_gt_u32 s45, 13
	s_barrier
	s_cbranch_scc0 .LBB0_1246
	v_lshl_add_u32 v134, s42, 8, v139
	v_ashrrev_i32_e32 v135, 31, v134
	v_lshlrev_b64 v[142:143], 11, v[134:135]
	v_mul_f32_e32 v135, 0xbfb8aa3b, v126
	v_exp_f32_e32 v135, v135
	v_lshl_or_b32 v136, s43, 7, v150
	v_ashrrev_i32_e32 v137, 31, v136
	v_lshl_add_u64 v[142:143], s[16:17], 0, v[142:143]
	v_add_f32_e32 v135, 1.0, v135
	v_rcp_f32_e32 v135, v135
	s_mov_b32 s0, 0x40000
	v_mov_b32_e32 v138, v153
	v_mov_b32_e32 v140, v152
	v_mul_f32_e32 v126, v126, v135
	v_mul_f32_e32 v122, v126, v122
	v_mul_f32_e32 v126, 0xbfb8aa3b, v127
	v_exp_f32_e32 v126, v126
	s_mov_b32 s43, s22
	s_mov_b32 s42, s41
	v_add_f32_e32 v126, 1.0, v126
	v_rcp_f32_e32 v126, v126
	s_nop 0
	v_mul_f32_e32 v126, v127, v126
	v_mul_f32_e32 v123, v126, v123
	v_mul_f32_e32 v126, 0xbfb8aa3b, v128
	v_exp_f32_e32 v126, v126
	s_nop 0
	v_add_f32_e32 v126, 1.0, v126
	v_rcp_f32_e32 v126, v126
	s_nop 0
	v_mul_f32_e32 v126, v128, v126
	v_mul_f32_e32 v124, v126, v124
	v_mul_f32_e32 v126, 0xbfb8aa3b, v129
	v_exp_f32_e32 v126, v126
	s_nop 0
	v_add_f32_e32 v126, 1.0, v126
	v_rcp_f32_e32 v126, v126
	s_nop 0
	v_mul_f32_e32 v126, v129, v126
	v_mul_f32_e32 v125, v126, v125
	v_mul_f32_e32 v126, 0xbfb8aa3b, v118
	v_exp_f32_e32 v126, v126
	s_nop 0
	v_add_f32_e32 v126, 1.0, v126
	v_rcp_f32_e32 v126, v126
	s_nop 0
	v_mul_f32_e32 v118, v118, v126
	v_mul_f32_e32 v126, v118, v114
	v_mul_f32_e32 v114, 0xbfb8aa3b, v119
	v_exp_f32_e32 v114, v114
	v_cvt_pk_bf16_f32 v118, v122, v123
	s_nop 0
	v_add_f32_e32 v114, 1.0, v114
	v_rcp_f32_e32 v114, v114
	s_nop 0
	v_mul_f32_e32 v114, v119, v114
	v_mul_f32_e32 v127, v114, v115
	v_mul_f32_e32 v114, 0xbfb8aa3b, v120
	v_exp_f32_e32 v114, v114
	v_cvt_pk_bf16_f32 v119, v124, v125
	s_nop 0
	v_add_f32_e32 v114, 1.0, v114
	v_rcp_f32_e32 v114, v114
	s_nop 0
	v_mul_f32_e32 v114, v120, v114
	v_mul_f32_e32 v128, v114, v116
	v_mul_f32_e32 v114, 0xbfb8aa3b, v121
	v_exp_f32_e32 v114, v114
	v_cvt_pk_bf16_f32 v120, v126, v127
	s_nop 0
	v_add_f32_e32 v114, 1.0, v114
	v_rcp_f32_e32 v114, v114
	s_nop 0
	v_mul_f32_e32 v114, v121, v114
	v_mul_f32_e32 v121, v114, v117
	v_lshlrev_b64 v[116:117], 1, v[136:137]
	v_lshl_add_u64 v[114:115], v[142:143], 0, v[116:117]
	v_cvt_pk_bf16_f32 v121, v128, v121
	s_cmp_eq_u32 s101, 1
	s_cbranch_scc1 .Lgs2_a_0
	global_store_dwordx4 v[114:115], v[118:121], off
	s_branch .Lgs2_b_0
.Lgs2_a_0:
	global_store_dwordx4 v[114:115], v[118:121], off sc1
.Lgs2_b_0:
	v_mov_b32_e32 v136, v154
	s_nop 0
	v_mul_f32_e32 v120, 0xbfb8aa3b, v110
	v_exp_f32_e32 v120, v120
	v_or_b32_e32 v118, 16, v134
	v_ashrrev_i32_e32 v119, 31, v118
	v_lshlrev_b64 v[118:119], 11, v[118:119]
	v_add_f32_e32 v120, 1.0, v120
	v_rcp_f32_e32 v120, v120
	v_lshl_add_u64 v[118:119], s[16:17], 0, v[118:119]
	v_mul_f32_e32 v110, v110, v120
	v_mul_f32_e32 v106, v110, v106
	v_mul_f32_e32 v110, 0xbfb8aa3b, v111
	v_exp_f32_e32 v110, v110
	s_nop 0
	v_add_f32_e32 v110, 1.0, v110
	v_rcp_f32_e32 v110, v110
	s_nop 0
	v_mul_f32_e32 v110, v111, v110
	v_mul_f32_e32 v107, v110, v107
	v_mul_f32_e32 v110, 0xbfb8aa3b, v112
	v_exp_f32_e32 v110, v110
	s_nop 0
	v_add_f32_e32 v110, 1.0, v110
	v_rcp_f32_e32 v110, v110
	s_nop 0
	v_mul_f32_e32 v110, v112, v110
	v_mul_f32_e32 v108, v110, v108
	v_mul_f32_e32 v110, 0xbfb8aa3b, v113
	v_exp_f32_e32 v110, v110
	s_nop 0
	v_add_f32_e32 v110, 1.0, v110
	v_rcp_f32_e32 v110, v110
	s_nop 0
	v_mul_f32_e32 v110, v113, v110
	v_mul_f32_e32 v109, v110, v109
	v_mul_f32_e32 v110, 0xbfb8aa3b, v102
	v_exp_f32_e32 v110, v110
	s_nop 0
	v_add_f32_e32 v110, 1.0, v110
	v_rcp_f32_e32 v110, v110
	s_nop 0
	v_mul_f32_e32 v102, v102, v110
	v_mul_f32_e32 v110, v102, v98
	v_mul_f32_e32 v98, 0xbfb8aa3b, v103
	v_exp_f32_e32 v98, v98
	s_nop 0
	v_add_f32_e32 v98, 1.0, v98
	v_rcp_f32_e32 v98, v98
	s_nop 0
	v_mul_f32_e32 v98, v103, v98
	v_mul_f32_e32 v111, v98, v99
	v_mul_f32_e32 v98, 0xbfb8aa3b, v104
	v_exp_f32_e32 v98, v98
	v_lshl_add_u64 v[102:103], v[118:119], 0, v[116:117]
	v_add_f32_e32 v98, 1.0, v98
	v_rcp_f32_e32 v98, v98
	s_nop 0
	v_mul_f32_e32 v98, v104, v98
	v_mul_f32_e32 v104, v98, v100
	v_mul_f32_e32 v98, 0xbfb8aa3b, v105
	v_exp_f32_e32 v98, v98
	s_nop 0
	v_add_f32_e32 v98, 1.0, v98
	v_rcp_f32_e32 v98, v98
	s_nop 0
	v_mul_f32_e32 v98, v105, v98
	v_mul_f32_e32 v101, v98, v101
	v_cvt_pk_bf16_f32 v98, v106, v107
	v_cvt_pk_bf16_f32 v99, v108, v109
	v_cvt_pk_bf16_f32 v100, v110, v111
	v_cvt_pk_bf16_f32 v101, v104, v101
	s_cmp_eq_u32 s101, 1
	s_cbranch_scc1 .Lgs2_a_1
	global_store_dwordx4 v[102:103], v[98:101], off
	s_branch .Lgs2_b_1
.Lgs2_a_1:
	global_store_dwordx4 v[102:103], v[98:101], off sc1
.Lgs2_b_1:
	s_nop 1
	v_mul_f32_e32 v100, 0xbfb8aa3b, v94
	v_exp_f32_e32 v100, v100
	v_or_b32_e32 v98, 32, v134
	v_ashrrev_i32_e32 v99, 31, v98
	v_lshlrev_b64 v[98:99], 11, v[98:99]
	v_add_f32_e32 v100, 1.0, v100
	v_rcp_f32_e32 v100, v100
	v_lshl_add_u64 v[98:99], s[16:17], 0, v[98:99]
	v_mul_f32_e32 v94, v94, v100
	v_mul_f32_e32 v90, v94, v90
	v_mul_f32_e32 v94, 0xbfb8aa3b, v95
	v_exp_f32_e32 v94, v94
	s_nop 0
	v_add_f32_e32 v94, 1.0, v94
	v_rcp_f32_e32 v94, v94
	s_nop 0
	v_mul_f32_e32 v94, v95, v94
	v_mul_f32_e32 v91, v94, v91
	v_mul_f32_e32 v94, 0xbfb8aa3b, v96
	v_exp_f32_e32 v94, v94
	s_nop 0
	v_add_f32_e32 v94, 1.0, v94
	v_rcp_f32_e32 v94, v94
	s_nop 0
	v_mul_f32_e32 v94, v96, v94
	v_mul_f32_e32 v92, v94, v92
	v_mul_f32_e32 v94, 0xbfb8aa3b, v97
	v_exp_f32_e32 v94, v94
	s_nop 0
	v_add_f32_e32 v94, 1.0, v94
	v_rcp_f32_e32 v94, v94
	s_nop 0
	v_mul_f32_e32 v94, v97, v94
	v_mul_f32_e32 v93, v94, v93
	v_mul_f32_e32 v94, 0xbfb8aa3b, v86
	v_exp_f32_e32 v94, v94
	s_nop 0
	v_add_f32_e32 v94, 1.0, v94
	v_rcp_f32_e32 v94, v94
	s_nop 0
	v_mul_f32_e32 v86, v86, v94
	v_mul_f32_e32 v94, v86, v82
	v_mul_f32_e32 v82, 0xbfb8aa3b, v87
	v_exp_f32_e32 v82, v82
	s_nop 0
	v_add_f32_e32 v82, 1.0, v82
	v_rcp_f32_e32 v82, v82
	s_nop 0
	v_mul_f32_e32 v82, v87, v82
	v_mul_f32_e32 v95, v82, v83
	v_mul_f32_e32 v82, 0xbfb8aa3b, v88
	v_exp_f32_e32 v82, v82
	v_lshl_add_u64 v[86:87], v[98:99], 0, v[116:117]
	v_add_f32_e32 v82, 1.0, v82
	v_rcp_f32_e32 v82, v82
	s_nop 0
	v_mul_f32_e32 v82, v88, v82
	v_mul_f32_e32 v88, v82, v84
	v_mul_f32_e32 v82, 0xbfb8aa3b, v89
	v_exp_f32_e32 v82, v82
	s_nop 0
	v_add_f32_e32 v82, 1.0, v82
	v_rcp_f32_e32 v82, v82
	s_nop 0
	v_mul_f32_e32 v82, v89, v82
	v_mul_f32_e32 v85, v82, v85
	v_cvt_pk_bf16_f32 v82, v90, v91
	v_cvt_pk_bf16_f32 v83, v92, v93
	v_cvt_pk_bf16_f32 v84, v94, v95
	v_cvt_pk_bf16_f32 v85, v88, v85
	s_cmp_eq_u32 s101, 1
	s_cbranch_scc1 .Lgs2_a_2
	global_store_dwordx4 v[86:87], v[82:85], off
	s_branch .Lgs2_b_2
.Lgs2_a_2:
	global_store_dwordx4 v[86:87], v[82:85], off sc1
.Lgs2_b_2:
	s_nop 1
	v_mul_f32_e32 v84, 0xbfb8aa3b, v78
	v_exp_f32_e32 v84, v84
	v_or_b32_e32 v82, 48, v134
	v_ashrrev_i32_e32 v83, 31, v82
	v_lshlrev_b64 v[82:83], 11, v[82:83]
	v_add_f32_e32 v84, 1.0, v84
	v_rcp_f32_e32 v84, v84
	v_lshl_add_u64 v[82:83], s[16:17], 0, v[82:83]
	v_mov_b32_e32 v134, v155
	v_mul_f32_e32 v78, v78, v84
	v_mul_f32_e32 v74, v78, v74
	v_mul_f32_e32 v78, 0xbfb8aa3b, v79
	v_exp_f32_e32 v78, v78
	s_nop 0
	v_add_f32_e32 v78, 1.0, v78
	v_rcp_f32_e32 v78, v78
	s_nop 0
	v_mul_f32_e32 v78, v79, v78
	v_mul_f32_e32 v75, v78, v75
	v_mul_f32_e32 v78, 0xbfb8aa3b, v80
	v_exp_f32_e32 v78, v78
	s_nop 0
	v_add_f32_e32 v78, 1.0, v78
	v_rcp_f32_e32 v78, v78
	s_nop 0
	v_mul_f32_e32 v78, v80, v78
	v_mul_f32_e32 v76, v78, v76
	v_mul_f32_e32 v78, 0xbfb8aa3b, v81
	v_exp_f32_e32 v78, v78
	s_nop 0
	v_add_f32_e32 v78, 1.0, v78
	v_rcp_f32_e32 v78, v78
	s_nop 0
	v_mul_f32_e32 v78, v81, v78
	v_mul_f32_e32 v77, v78, v77
	v_mul_f32_e32 v78, 0xbfb8aa3b, v70
	v_exp_f32_e32 v78, v78
	s_nop 0
	v_add_f32_e32 v78, 1.0, v78
	v_rcp_f32_e32 v78, v78
	s_nop 0
	v_mul_f32_e32 v70, v70, v78
	v_mul_f32_e32 v78, v70, v66
	v_mul_f32_e32 v66, 0xbfb8aa3b, v71
	v_exp_f32_e32 v66, v66
	s_nop 0
	v_add_f32_e32 v66, 1.0, v66
	v_rcp_f32_e32 v66, v66
	s_nop 0
	v_mul_f32_e32 v66, v71, v66
	v_mul_f32_e32 v79, v66, v67
	v_mul_f32_e32 v66, 0xbfb8aa3b, v72
	v_exp_f32_e32 v66, v66
	v_lshl_add_u64 v[70:71], v[82:83], 0, v[116:117]
	v_add_f32_e32 v66, 1.0, v66
	v_rcp_f32_e32 v66, v66
	s_nop 0
	v_mul_f32_e32 v66, v72, v66
	v_mul_f32_e32 v72, v66, v68
	v_mul_f32_e32 v66, 0xbfb8aa3b, v73
	v_exp_f32_e32 v66, v66
	s_nop 0
	v_add_f32_e32 v66, 1.0, v66
	v_rcp_f32_e32 v66, v66
	s_nop 0
	v_mul_f32_e32 v66, v73, v66
	v_mul_f32_e32 v69, v66, v69
	v_cvt_pk_bf16_f32 v66, v74, v75
	v_cvt_pk_bf16_f32 v67, v76, v77
	v_cvt_pk_bf16_f32 v68, v78, v79
	v_cvt_pk_bf16_f32 v69, v72, v69
	s_cmp_eq_u32 s101, 1
	s_cbranch_scc1 .Lgs2_a_3
	global_store_dwordx4 v[70:71], v[66:69], off
	s_branch .Lgs2_b_3
.Lgs2_a_3:
	global_store_dwordx4 v[70:71], v[66:69], off sc1
.Lgs2_b_3:
	s_nop 1
	v_mul_f32_e32 v66, 0xbfb8aa3b, v58
	v_exp_f32_e32 v66, v66
	s_nop 0
	v_add_f32_e32 v66, 1.0, v66
	v_rcp_f32_e32 v66, v66
	s_nop 0
	v_mul_f32_e32 v58, v58, v66
	v_mul_f32_e32 v58, v58, v62
	v_mul_f32_e32 v62, 0xbfb8aa3b, v59
	v_exp_f32_e32 v62, v62
	s_nop 0
	v_add_f32_e32 v62, 1.0, v62
	v_rcp_f32_e32 v62, v62
	s_nop 0
	v_mul_f32_e32 v59, v59, v62
	v_mul_f32_e32 v62, 0xbfb8aa3b, v60
	v_exp_f32_e32 v62, v62
	v_mul_f32_e32 v59, v59, v63
	v_add_f32_e32 v62, 1.0, v62
	v_rcp_f32_e32 v62, v62
	s_nop 0
	v_mul_f32_e32 v60, v60, v62
	v_mul_f32_e32 v62, 0xbfb8aa3b, v61
	v_exp_f32_e32 v62, v62
	v_mul_f32_e32 v60, v60, v64
	v_add_f32_e32 v62, 1.0, v62
	v_rcp_f32_e32 v62, v62
	s_nop 0
	v_mul_f32_e32 v61, v61, v62
	v_mul_f32_e32 v62, 0xbfb8aa3b, v50
	v_exp_f32_e32 v62, v62
	v_mul_f32_e32 v61, v61, v65
	v_add_f32_e32 v62, 1.0, v62
	v_rcp_f32_e32 v62, v62
	s_nop 0
	v_mul_f32_e32 v50, v50, v62
	v_mul_f32_e32 v54, v50, v54
	v_mul_f32_e32 v50, 0xbfb8aa3b, v51
	v_exp_f32_e32 v50, v50
	s_nop 0
	v_add_f32_e32 v50, 1.0, v50
	v_rcp_f32_e32 v50, v50
	s_nop 0
	v_mul_f32_e32 v50, v51, v50
	v_mul_f32_e32 v55, v50, v55
	v_mul_f32_e32 v50, 0xbfb8aa3b, v52
	v_exp_f32_e32 v50, v50
	s_nop 0
	v_add_f32_e32 v50, 1.0, v50
	v_rcp_f32_e32 v50, v50
	s_nop 0
	v_mul_f32_e32 v50, v52, v50
	v_mul_f32_e32 v56, v50, v56
	v_mul_f32_e32 v50, 0xbfb8aa3b, v53
	v_exp_f32_e32 v50, v50
	s_nop 0
	v_add_f32_e32 v50, 1.0, v50
	v_rcp_f32_e32 v50, v50
	s_nop 0
	v_mul_f32_e32 v50, v53, v50
	v_mul_f32_e32 v53, v50, v57
	v_cvt_pk_bf16_f32 v50, v58, v59
	v_cvt_pk_bf16_f32 v51, v60, v61
	v_cvt_pk_bf16_f32 v52, v54, v55
	v_add_co_u32_e32 v54, vcc, s0, v114
	v_cvt_pk_bf16_f32 v53, v56, v53
	s_mov_b32 s0, 0x48000
	s_nop 0
	v_addc_co_u32_e32 v55, vcc, 0, v115, vcc
	s_cmp_eq_u32 s101, 1
	s_cbranch_scc1 .Lgs2_a_4
	global_store_dwordx4 v[54:55], v[50:53], off
	s_branch .Lgs2_b_4
.Lgs2_a_4:
	global_store_dwordx4 v[54:55], v[50:53], off sc1
.Lgs2_b_4:
	s_nop 1
	v_mul_f32_e32 v50, 0xbfb8aa3b, v42
	v_exp_f32_e32 v50, v50
	s_nop 0
	v_add_f32_e32 v50, 1.0, v50
	v_rcp_f32_e32 v50, v50
	s_nop 0
	v_mul_f32_e32 v42, v42, v50
	v_mul_f32_e32 v42, v42, v46
	v_mul_f32_e32 v46, 0xbfb8aa3b, v43
	v_exp_f32_e32 v46, v46
	s_nop 0
	v_add_f32_e32 v46, 1.0, v46
	v_rcp_f32_e32 v46, v46
	s_nop 0
	v_mul_f32_e32 v43, v43, v46
	v_mul_f32_e32 v46, 0xbfb8aa3b, v44
	v_exp_f32_e32 v46, v46
	v_mul_f32_e32 v43, v43, v47
	v_add_f32_e32 v46, 1.0, v46
	v_rcp_f32_e32 v46, v46
	s_nop 0
	v_mul_f32_e32 v44, v44, v46
	v_mul_f32_e32 v46, 0xbfb8aa3b, v45
	v_exp_f32_e32 v46, v46
	v_mul_f32_e32 v44, v44, v48
	v_add_f32_e32 v46, 1.0, v46
	v_rcp_f32_e32 v46, v46
	s_nop 0
	v_mul_f32_e32 v45, v45, v46
	v_mul_f32_e32 v46, 0xbfb8aa3b, v34
	v_exp_f32_e32 v46, v46
	v_mul_f32_e32 v45, v45, v49
	v_add_f32_e32 v46, 1.0, v46
	v_rcp_f32_e32 v46, v46
	s_nop 0
	v_mul_f32_e32 v34, v34, v46
	v_mul_f32_e32 v38, v34, v38
	v_mul_f32_e32 v34, 0xbfb8aa3b, v35
	v_exp_f32_e32 v34, v34
	s_nop 0
	v_add_f32_e32 v34, 1.0, v34
	v_rcp_f32_e32 v34, v34
	s_nop 0
	v_mul_f32_e32 v34, v35, v34
	v_mul_f32_e32 v39, v34, v39
	v_mul_f32_e32 v34, 0xbfb8aa3b, v36
	v_exp_f32_e32 v34, v34
	s_nop 0
	v_add_f32_e32 v34, 1.0, v34
	v_rcp_f32_e32 v34, v34
	s_nop 0
	v_mul_f32_e32 v34, v36, v34
	v_mul_f32_e32 v40, v34, v40
	v_mul_f32_e32 v34, 0xbfb8aa3b, v37
	v_exp_f32_e32 v34, v34
	s_nop 0
	v_add_f32_e32 v34, 1.0, v34
	v_rcp_f32_e32 v34, v34
	s_nop 0
	v_mul_f32_e32 v34, v37, v34
	v_mul_f32_e32 v37, v34, v41
	v_cvt_pk_bf16_f32 v34, v42, v43
	v_cvt_pk_bf16_f32 v35, v44, v45
	v_cvt_pk_bf16_f32 v36, v38, v39
	v_add_co_u32_e32 v38, vcc, s0, v114
	v_cvt_pk_bf16_f32 v37, v40, v37
	s_mov_b32 s0, 0x50000
	s_nop 0
	v_addc_co_u32_e32 v39, vcc, 0, v115, vcc
	s_cmp_eq_u32 s101, 1
	s_cbranch_scc1 .Lgs2_a_5
	global_store_dwordx4 v[38:39], v[34:37], off
	s_branch .Lgs2_b_5
.Lgs2_a_5:
	global_store_dwordx4 v[38:39], v[34:37], off sc1
.Lgs2_b_5:
	s_nop 1
	v_mul_f32_e32 v34, 0xbfb8aa3b, v26
	v_exp_f32_e32 v34, v34
	s_nop 0
	v_add_f32_e32 v34, 1.0, v34
	v_rcp_f32_e32 v34, v34
	s_nop 0
	v_mul_f32_e32 v26, v26, v34
	v_mul_f32_e32 v26, v26, v30
	v_mul_f32_e32 v30, 0xbfb8aa3b, v27
	v_exp_f32_e32 v30, v30
	s_nop 0
	v_add_f32_e32 v30, 1.0, v30
	v_rcp_f32_e32 v30, v30
	s_nop 0
	v_mul_f32_e32 v27, v27, v30
	v_mul_f32_e32 v30, 0xbfb8aa3b, v28
	v_exp_f32_e32 v30, v30
	v_mul_f32_e32 v27, v27, v31
	v_add_f32_e32 v30, 1.0, v30
	v_rcp_f32_e32 v30, v30
	s_nop 0
	v_mul_f32_e32 v28, v28, v30
	v_mul_f32_e32 v30, 0xbfb8aa3b, v29
	v_exp_f32_e32 v30, v30
	v_mul_f32_e32 v28, v28, v32
	v_add_f32_e32 v30, 1.0, v30
	v_rcp_f32_e32 v30, v30
	s_nop 0
	v_mul_f32_e32 v29, v29, v30
	v_mul_f32_e32 v30, 0xbfb8aa3b, v18
	v_exp_f32_e32 v30, v30
	v_mul_f32_e32 v29, v29, v33
	v_add_f32_e32 v30, 1.0, v30
	v_rcp_f32_e32 v30, v30
	s_nop 0
	v_mul_f32_e32 v18, v18, v30
	v_mul_f32_e32 v22, v18, v22
	v_mul_f32_e32 v18, 0xbfb8aa3b, v19
	v_exp_f32_e32 v18, v18
	s_nop 0
	v_add_f32_e32 v18, 1.0, v18
	v_rcp_f32_e32 v18, v18
	s_nop 0
	v_mul_f32_e32 v18, v19, v18
	v_mul_f32_e32 v23, v18, v23
	v_mul_f32_e32 v18, 0xbfb8aa3b, v20
	v_exp_f32_e32 v18, v18
	s_nop 0
	v_add_f32_e32 v18, 1.0, v18
	v_rcp_f32_e32 v18, v18
	s_nop 0
	v_mul_f32_e32 v18, v20, v18
	v_mul_f32_e32 v24, v18, v24
	v_mul_f32_e32 v18, 0xbfb8aa3b, v21
	v_exp_f32_e32 v18, v18
	s_nop 0
	v_add_f32_e32 v18, 1.0, v18
	v_rcp_f32_e32 v18, v18
	s_nop 0
	v_mul_f32_e32 v18, v21, v18
	v_mul_f32_e32 v21, v18, v25
	v_cvt_pk_bf16_f32 v18, v26, v27
	v_cvt_pk_bf16_f32 v19, v28, v29
	v_cvt_pk_bf16_f32 v20, v22, v23
	v_add_co_u32_e32 v22, vcc, s0, v114
	v_cvt_pk_bf16_f32 v21, v24, v21
	s_mov_b64 s[0:1], s[8:9]
	s_nop 0
	v_addc_co_u32_e32 v23, vcc, 0, v115, vcc
	s_cmp_eq_u32 s101, 1
	s_cbranch_scc1 .Lgs2_a_6
	global_store_dwordx4 v[22:23], v[18:21], off
	s_branch .Lgs2_b_6
.Lgs2_a_6:
	global_store_dwordx4 v[22:23], v[18:21], off sc1
.Lgs2_b_6:
	s_nop 1
	v_mul_f32_e32 v18, 0xbfb8aa3b, v6
	v_exp_f32_e32 v18, v18
	s_nop 0
	v_add_f32_e32 v18, 1.0, v18
	v_rcp_f32_e32 v18, v18
	s_nop 0
	v_mul_f32_e32 v6, v6, v18
	v_mul_f32_e32 v6, v6, v14
	v_mul_f32_e32 v14, 0xbfb8aa3b, v7
	v_exp_f32_e32 v14, v14
	s_nop 0
	v_add_f32_e32 v14, 1.0, v14
	v_rcp_f32_e32 v14, v14
	s_nop 0
	v_mul_f32_e32 v7, v7, v14
	v_mul_f32_e32 v14, 0xbfb8aa3b, v8
	v_exp_f32_e32 v14, v14
	v_mul_f32_e32 v7, v7, v15
	v_add_f32_e32 v14, 1.0, v14
	v_rcp_f32_e32 v14, v14
	s_nop 0
	v_mul_f32_e32 v8, v8, v14
	v_mul_f32_e32 v14, 0xbfb8aa3b, v9
	v_exp_f32_e32 v14, v14
	v_mul_f32_e32 v8, v8, v16
	v_add_f32_e32 v14, 1.0, v14
	v_rcp_f32_e32 v14, v14
	s_nop 0
	v_mul_f32_e32 v9, v9, v14
	v_mul_f32_e32 v14, 0xbfb8aa3b, v2
	v_exp_f32_e32 v14, v14
	v_mul_f32_e32 v9, v9, v17
	v_add_f32_e32 v14, 1.0, v14
	v_rcp_f32_e32 v14, v14
	s_nop 0
	v_mul_f32_e32 v2, v2, v14
	v_mul_f32_e32 v10, v2, v10
	v_mul_f32_e32 v2, 0xbfb8aa3b, v3
	v_exp_f32_e32 v2, v2
	s_nop 0
	v_add_f32_e32 v2, 1.0, v2
	v_rcp_f32_e32 v2, v2
	s_nop 0
	v_mul_f32_e32 v2, v3, v2
	v_mul_f32_e32 v11, v2, v11
	v_mul_f32_e32 v2, 0xbfb8aa3b, v4
	v_exp_f32_e32 v2, v2
	s_nop 0
	v_add_f32_e32 v2, 1.0, v2
	v_rcp_f32_e32 v2, v2
	s_nop 0
	v_mul_f32_e32 v2, v4, v2
	v_mul_f32_e32 v12, v2, v12
	v_mul_f32_e32 v2, 0xbfb8aa3b, v5
	v_exp_f32_e32 v2, v2
	s_nop 0
	v_add_f32_e32 v2, 1.0, v2
	v_rcp_f32_e32 v2, v2
	s_nop 0
	v_mul_f32_e32 v2, v5, v2
	v_mul_f32_e32 v5, v2, v13
	v_cvt_pk_bf16_f32 v2, v6, v7
	v_add_co_u32_e32 v6, vcc, 0x58000, v114
	v_cvt_pk_bf16_f32 v3, v8, v9
	v_cvt_pk_bf16_f32 v4, v10, v11
	v_cvt_pk_bf16_f32 v5, v12, v5
	s_nop 1
	v_addc_co_u32_e32 v7, vcc, 0, v115, vcc
	s_and_b64 vcc, exec, s[4:5]
	s_cmp_eq_u32 s101, 1
	s_cbranch_scc1 .Lgs2_a_7
	global_store_dwordx4 v[6:7], v[2:5], off
	s_branch .Lgs2_b_7
.Lgs2_a_7:
	global_store_dwordx4 v[6:7], v[2:5], off sc1
.Lgs2_b_7:
	s_cbranch_vccz .LBB0_1233
	s_branch .LBB0_1252

.LBB0_1318:
	s_add_i32 s44, s44, 1
	s_mul_i32 s4, s44, s43
	s_mul_hi_u32 s5, s44, s79
	s_add_i32 s5, s5, s4
	s_mul_i32 s4, s44, s79
	s_add_u32 s20, s4, s29
	s_addc_u32 s21, s5, s34
	s_cmp_ge_u32 s20, s16
	s_cselect_b32 s101, 1, 0
	v_mov_b64_e32 v[2:3], s[16:17]
	v_cmp_ge_i64_e64 s[4:5], s[20:21], v[2:3]
	v_cmp_lt_i64_e64 s[6:7], s[20:21], v[2:3]
	s_and_b64 vcc, exec, s[4:5]
	s_cbranch_vccnz .LBB0_1320
	s_ashr_i32 s18, s20, 31
	s_lshr_b32 s18, s18, 29
	s_add_i32 s18, s20, s18
	s_ashr_i32 s19, s18, 3
	s_and_b32 s18, s18, -8
	s_sub_i32 s18, s20, s18
	s_cmp_lt_i32 s18, 0
	s_cselect_b32 s20, s35, s31
	s_mul_i32 s18, s20, s18
	s_add_i32 s18, s18, s19
	s_ashr_i32 s19, s18, 31
	s_lshr_b32 s19, s19, 27
	s_add_i32 s19, s18, s19
	s_ashr_i32 s20, s19, 5
	s_lshl_b32 s20, s20, 3
	s_sub_i32 s21, s28, s20
	s_min_i32 s21, s21, 8
	s_abs_i32 s24, s21
	v_cvt_f32_u32_e32 v2, s24
	s_sub_i32 s26, 0, s24
	s_andn2_b32 s19, s19, 31
	s_sub_i32 s19, s18, s19
	v_rcp_iflag_f32_e32 v2, v2
	s_abs_i32 s18, s19
	s_xor_b32 s25, s19, s21
	s_ashr_i32 s25, s25, 31
	v_mul_f32_e32 v2, 0x4f7ffffe, v2
	v_cvt_u32_f32_e32 v2, v2
	s_nop 0
	v_readfirstlane_b32 s27, v2
	s_mul_i32 s26, s26, s27
	s_mul_hi_u32 s26, s27, s26
	s_add_i32 s27, s27, s26
	s_mul_hi_u32 s26, s18, s27
	s_mul_i32 s27, s26, s24
	s_sub_i32 s18, s18, s27
	s_add_i32 s33, s26, 1
	s_sub_i32 s27, s18, s24
	s_cmp_ge_u32 s18, s24
	s_cselect_b32 s26, s33, s26
	s_cselect_b32 s18, s27, s18
	s_add_i32 s27, s26, 1
	s_cmp_ge_u32 s18, s24
	s_cselect_b32 s18, s27, s26
	s_xor_b32 s18, s18, s25
	s_sub_i32 s18, s18, s25
	s_mul_i32 s21, s18, s21
	s_sub_i32 s19, s19, s21
	s_add_i32 s45, s19, s20

.LBB0_1327:
	s_add_u32 s24, s8, s22
	s_addc_u32 s25, s9, s23
	s_add_u32 s26, s24, 0x100
	s_addc_u32 s27, s25, 0
	s_add_u32 s33, s19, s22
	s_addc_u32 s52, s48, s23
	s_cmpk_eq_i32 s22, 0x700
	s_cselect_b64 s[50:51], -1, 0
	s_and_b64 s[24:25], s[50:51], exec
	s_cselect_b32 s27, s9, s27
	s_cselect_b32 s26, s8, s26
	s_cselect_b32 s25, s21, s52
	s_cselect_b32 s24, s20, s33
	s_add_i32 s33, 0, 0x10000
	v_add_u32_e32 v137, s33, v148
	ds_read_b128 v[156:159], v137
	ds_read_b128 v[160:163], v137 offset:1024
	ds_read_b128 v[172:175], v137 offset:2048
	ds_read_b128 v[176:179], v137 offset:3072
	s_and_b64 vcc, s[6:7], s[50:51]
	v_cndmask_b32_e32 v226, v134, v151, vcc
	v_cndmask_b32_e32 v164, v136, v152, vcc
	v_cndmask_b32_e32 v137, v140, v153, vcc
	v_cndmask_b32_e32 v139, v138, v154, vcc
	v_lshl_add_u64 v[166:167], v[144:145], 0, s[22:23]
	s_add_i32 m0, s37, 0xc000
	ds_read_b128 v[180:183], v150
	ds_read_b128 v[184:187], v150 offset:1024
	ds_read_b128 v[188:191], v150 offset:2048
	ds_read_b128 v[192:195], v150 offset:3072
	ds_read_b128 v[196:199], v150 offset:4096
	ds_read_b128 v[200:203], v150 offset:5120
	ds_read_b128 v[204:207], v150 offset:6144
	ds_read_b128 v[208:211], v150 offset:7168
	global_load_lds_dwordx4 v[166:167], off
	v_lshl_add_u64 v[166:167], v[142:143], 0, s[22:23]
	s_add_i32 m0, s37, 0xe000
	s_nop 0
	global_load_lds_dwordx4 v[166:167], off
	s_waitcnt lgkmcnt(8)
	s_barrier
	s_waitcnt lgkmcnt(0)
	s_setprio 1
	s_waitcnt lgkmcnt(0)
	v_mfma_f32_16x16x32_bf16 v[126:129], v[156:159], v[180:183], v[126:129]
	v_mfma_f32_16x16x32_bf16 v[122:125], v[172:175], v[180:183], v[122:125]
	v_mfma_f32_16x16x32_bf16 v[114:117], v[156:159], v[188:191], v[114:117]
	v_mfma_f32_16x16x32_bf16 v[106:109], v[172:175], v[188:191], v[106:109]
	v_mfma_f32_16x16x32_bf16 v[98:101], v[156:159], v[196:199], v[98:101]
	v_mfma_f32_16x16x32_bf16 v[90:93], v[172:175], v[196:199], v[90:93]
	v_mfma_f32_16x16x32_bf16 v[82:85], v[156:159], v[204:207], v[82:85]
	v_mfma_f32_16x16x32_bf16 v[74:77], v[172:175], v[204:207], v[74:77]
	v_mfma_f32_16x16x32_bf16 v[126:129], v[160:163], v[184:187], v[126:129]
	v_mfma_f32_16x16x32_bf16 v[122:125], v[176:179], v[184:187], v[122:125]
	v_mfma_f32_16x16x32_bf16 v[114:117], v[160:163], v[192:195], v[114:117]
	v_mfma_f32_16x16x32_bf16 v[106:109], v[176:179], v[192:195], v[106:109]
	v_mfma_f32_16x16x32_bf16 v[98:101], v[160:163], v[200:203], v[98:101]
	v_mfma_f32_16x16x32_bf16 v[90:93], v[176:179], v[200:203], v[90:93]
	v_mfma_f32_16x16x32_bf16 v[82:85], v[160:163], v[208:211], v[82:85]
	v_mfma_f32_16x16x32_bf16 v[74:77], v[176:179], v[208:211], v[74:77]
	s_setprio 0
	s_barrier
	s_add_i32 s52, 0, 0x14000
	s_add_i32 s33, s33, s36
	v_add_u32_e32 v141, s52, v148
	v_lshl_add_u64 v[166:167], s[24:25], 0, v[130:131]
	s_mov_b32 m0, s33
	ds_read_b128 v[212:215], v141
	ds_read_b128 v[230:233], v141 offset:1024
	ds_read_b128 v[234:237], v141 offset:2048
	ds_read_b128 v[238:241], v141 offset:3072
	global_load_lds_dwordx4 v[166:167], off
	v_lshl_add_u64 v[220:221], s[24:25], 0, v[132:133]
	s_add_i32 m0, s33, 0x2000
	s_nop 0
	global_load_lds_dwordx4 v[220:221], off
	s_barrier
	s_waitcnt lgkmcnt(0)
	s_setprio 1
	s_waitcnt lgkmcnt(0)
	v_mfma_f32_16x16x32_bf16 v[118:121], v[212:215], v[180:183], v[118:121]
	v_mfma_f32_16x16x32_bf16 v[110:113], v[234:237], v[180:183], v[110:113]
	v_mfma_f32_16x16x32_bf16 v[102:105], v[212:215], v[188:191], v[102:105]
	v_mfma_f32_16x16x32_bf16 v[94:97], v[234:237], v[188:191], v[94:97]
	v_mfma_f32_16x16x32_bf16 v[86:89], v[212:215], v[196:199], v[86:89]
	v_mfma_f32_16x16x32_bf16 v[78:81], v[234:237], v[196:199], v[78:81]
	v_mfma_f32_16x16x32_bf16 v[70:73], v[212:215], v[204:207], v[70:73]
	v_mfma_f32_16x16x32_bf16 v[58:61], v[234:237], v[204:207], v[58:61]
	v_mfma_f32_16x16x32_bf16 v[118:121], v[230:233], v[184:187], v[118:121]
	v_mfma_f32_16x16x32_bf16 v[110:113], v[238:241], v[184:187], v[110:113]
	v_mfma_f32_16x16x32_bf16 v[102:105], v[230:233], v[192:195], v[102:105]
	v_mfma_f32_16x16x32_bf16 v[94:97], v[238:241], v[192:195], v[94:97]
	v_mfma_f32_16x16x32_bf16 v[86:89], v[230:233], v[200:203], v[86:89]
	v_mfma_f32_16x16x32_bf16 v[78:81], v[238:241], v[200:203], v[78:81]
	v_mfma_f32_16x16x32_bf16 v[70:73], v[230:233], v[208:211], v[70:73]
	v_mfma_f32_16x16x32_bf16 v[58:61], v[238:241], v[208:211], v[58:61]
	s_setprio 0
	s_mov_b32 m0, s37
	s_barrier
	ds_read_b128 v[180:183], v150 offset:16384
	ds_read_b128 v[184:187], v150 offset:17408
	ds_read_b128 v[188:191], v150 offset:18432
	ds_read_b128 v[192:195], v150 offset:19456
	ds_read_b128 v[196:199], v150 offset:20480
	ds_read_b128 v[200:203], v150 offset:21504
	ds_read_b128 v[204:207], v150 offset:22528
	ds_read_b128 v[208:211], v150 offset:23552
	global_load_lds_dwordx4 v226, s[26:27]
	s_mov_b32 m0, s38
	v_mov_b32_e32 v165, v227
	global_load_lds_dwordx4 v164, s[26:27]
	s_barrier
	s_waitcnt lgkmcnt(0)
	v_lshl_add_u64 v[222:223], s[26:27], 0, v[226:227]
	v_lshl_add_u64 v[164:165], s[26:27], 0, v[164:165]
	s_setprio 1
	s_waitcnt lgkmcnt(0)
	v_mfma_f32_16x16x32_bf16 v[54:57], v[156:159], v[180:183], v[54:57]
	v_mfma_f32_16x16x32_bf16 v[50:53], v[172:175], v[180:183], v[50:53]
	v_mfma_f32_16x16x32_bf16 v[30:33], v[156:159], v[188:191], v[30:33]
	v_mfma_f32_16x16x32_bf16 v[26:29], v[172:175], v[188:191], v[26:29]
	v_mfma_f32_16x16x32_bf16 v[14:17], v[156:159], v[196:199], v[14:17]
	v_mfma_f32_16x16x32_bf16 v[10:13], v[172:175], v[196:199], v[10:13]
	v_mfma_f32_16x16x32_bf16 v[6:9], v[156:159], v[204:207], v[6:9]
	v_mfma_f32_16x16x32_bf16 v[2:5], v[172:175], v[204:207], v[2:5]
	v_mfma_f32_16x16x32_bf16 v[54:57], v[160:163], v[184:187], v[54:57]
	v_mfma_f32_16x16x32_bf16 v[50:53], v[176:179], v[184:187], v[50:53]
	v_mfma_f32_16x16x32_bf16 v[30:33], v[160:163], v[192:195], v[30:33]
	v_mfma_f32_16x16x32_bf16 v[26:29], v[176:179], v[192:195], v[26:29]
	v_mfma_f32_16x16x32_bf16 v[14:17], v[160:163], v[200:203], v[14:17]
	v_mfma_f32_16x16x32_bf16 v[10:13], v[176:179], v[200:203], v[10:13]
	v_mfma_f32_16x16x32_bf16 v[6:9], v[160:163], v[208:211], v[6:9]
	v_mfma_f32_16x16x32_bf16 v[2:5], v[176:179], v[208:211], v[2:5]
	s_setprio 0
	s_barrier
	s_add_u32 s50, s24, 0x40000
	s_addc_u32 s51, s25, 0
	s_add_i32 s33, s52, s36
	v_lshl_add_u64 v[156:157], s[50:51], 0, v[130:131]
	s_mov_b32 m0, s33
	s_nop 0
	global_load_lds_dwordx4 v[156:157], off
	v_lshl_add_u64 v[156:157], s[50:51], 0, v[132:133]
	s_add_i32 m0, s33, 0x2000
	s_nop 0
	global_load_lds_dwordx4 v[156:157], off
	s_waitcnt vmcnt(6)
	s_barrier
	s_setprio 1
	v_mfma_f32_16x16x32_bf16 v[62:65], v[212:215], v[180:183], v[62:65]
	v_mfma_f32_16x16x32_bf16 v[66:69], v[234:237], v[180:183], v[66:69]
	v_mfma_f32_16x16x32_bf16 v[42:45], v[212:215], v[188:191], v[42:45]
	v_mfma_f32_16x16x32_bf16 v[46:49], v[234:237], v[188:191], v[46:49]
	v_mfma_f32_16x16x32_bf16 v[34:37], v[212:215], v[196:199], v[34:37]
	v_mfma_f32_16x16x32_bf16 v[38:41], v[234:237], v[196:199], v[38:41]
	v_mfma_f32_16x16x32_bf16 v[18:21], v[212:215], v[204:207], v[18:21]
	v_mfma_f32_16x16x32_bf16 v[22:25], v[234:237], v[204:207], v[22:25]
	v_mfma_f32_16x16x32_bf16 v[62:65], v[230:233], v[184:187], v[62:65]
	v_mfma_f32_16x16x32_bf16 v[66:69], v[238:241], v[184:187], v[66:69]
	v_mfma_f32_16x16x32_bf16 v[42:45], v[230:233], v[192:195], v[42:45]
	v_mfma_f32_16x16x32_bf16 v[46:49], v[238:241], v[192:195], v[46:49]
	v_mfma_f32_16x16x32_bf16 v[34:37], v[230:233], v[200:203], v[34:37]
	v_mfma_f32_16x16x32_bf16 v[38:41], v[238:241], v[200:203], v[38:41]
	v_mfma_f32_16x16x32_bf16 v[18:21], v[230:233], v[208:211], v[18:21]
	v_mfma_f32_16x16x32_bf16 v[22:25], v[238:241], v[208:211], v[22:25]
	s_setprio 0
	s_add_i32 s33, 0, 0x18000
	v_add_u32_e32 v141, s33, v148
	s_barrier
	ds_read_b128 v[156:159], v141
	ds_read_b128 v[160:163], v141 offset:1024
	ds_read_b128 v[172:175], v141 offset:2048
	ds_read_b128 v[176:179], v141 offset:3072
	s_mov_b32 m0, s39
	ds_read_b128 v[180:183], v150 offset:32768
	ds_read_b128 v[184:187], v150 offset:33792
	ds_read_b128 v[188:191], v150 offset:34816
	ds_read_b128 v[192:195], v150 offset:35840
	ds_read_b128 v[196:199], v150 offset:36864
	ds_read_b128 v[200:203], v150 offset:37888
	ds_read_b128 v[204:207], v150 offset:38912
	ds_read_b128 v[208:211], v150 offset:39936
	global_load_lds_dwordx4 v137, s[26:27]
	s_mov_b32 m0, s40
	s_nop 0
	global_load_lds_dwordx4 v139, s[26:27]
	s_waitcnt lgkmcnt(8)
	s_barrier
	s_waitcnt lgkmcnt(0)
	s_setprio 1
	s_waitcnt lgkmcnt(0)
	v_mfma_f32_16x16x32_bf16 v[126:129], v[156:159], v[180:183], v[126:129]
	v_mfma_f32_16x16x32_bf16 v[122:125], v[172:175], v[180:183], v[122:125]
	v_mfma_f32_16x16x32_bf16 v[114:117], v[156:159], v[188:191], v[114:117]
	v_mfma_f32_16x16x32_bf16 v[106:109], v[172:175], v[188:191], v[106:109]
	v_mfma_f32_16x16x32_bf16 v[98:101], v[156:159], v[196:199], v[98:101]
	v_mfma_f32_16x16x32_bf16 v[90:93], v[172:175], v[196:199], v[90:93]
	v_mfma_f32_16x16x32_bf16 v[82:85], v[156:159], v[204:207], v[82:85]
	v_mfma_f32_16x16x32_bf16 v[74:77], v[172:175], v[204:207], v[74:77]
	v_mfma_f32_16x16x32_bf16 v[126:129], v[160:163], v[184:187], v[126:129]
	v_mfma_f32_16x16x32_bf16 v[122:125], v[176:179], v[184:187], v[122:125]
	v_mfma_f32_16x16x32_bf16 v[114:117], v[160:163], v[192:195], v[114:117]
	v_mfma_f32_16x16x32_bf16 v[106:109], v[176:179], v[192:195], v[106:109]
	v_mfma_f32_16x16x32_bf16 v[98:101], v[160:163], v[200:203], v[98:101]
	v_mfma_f32_16x16x32_bf16 v[90:93], v[176:179], v[200:203], v[90:93]
	v_mfma_f32_16x16x32_bf16 v[82:85], v[160:163], v[208:211], v[82:85]
	v_mfma_f32_16x16x32_bf16 v[74:77], v[176:179], v[208:211], v[74:77]
	s_setprio 0
	s_barrier
	s_add_i32 s26, 0, 0x1c000
	s_add_i32 s27, s33, s36
	v_add_u32_e32 v137, s26, v148
	v_lshl_add_u64 v[166:167], v[166:167], 0, s[96:97]
	s_mov_b32 m0, s27
	ds_read_b128 v[212:215], v137
	ds_read_b128 v[230:233], v137 offset:1024
	ds_read_b128 v[234:237], v137 offset:2048
	ds_read_b128 v[238:241], v137 offset:3072
	global_load_lds_dwordx4 v[166:167], off
	v_lshl_add_u64 v[166:167], v[220:221], 0, s[96:97]
	s_add_i32 m0, s27, 0x2000
	s_nop 0
	global_load_lds_dwordx4 v[166:167], off
	s_barrier
	s_waitcnt lgkmcnt(0)
	s_setprio 1
	s_waitcnt lgkmcnt(0)
	v_mfma_f32_16x16x32_bf16 v[118:121], v[212:215], v[180:183], v[118:121]
	v_mfma_f32_16x16x32_bf16 v[110:113], v[234:237], v[180:183], v[110:113]
	v_mfma_f32_16x16x32_bf16 v[102:105], v[212:215], v[188:191], v[102:105]
	v_mfma_f32_16x16x32_bf16 v[94:97], v[234:237], v[188:191], v[94:97]
	v_mfma_f32_16x16x32_bf16 v[86:89], v[212:215], v[196:199], v[86:89]
	v_mfma_f32_16x16x32_bf16 v[78:81], v[234:237], v[196:199], v[78:81]
	v_mfma_f32_16x16x32_bf16 v[70:73], v[212:215], v[204:207], v[70:73]
	v_mfma_f32_16x16x32_bf16 v[58:61], v[234:237], v[204:207], v[58:61]
	v_mfma_f32_16x16x32_bf16 v[118:121], v[230:233], v[184:187], v[118:121]
	v_mfma_f32_16x16x32_bf16 v[110:113], v[238:241], v[184:187], v[110:113]
	v_mfma_f32_16x16x32_bf16 v[102:105], v[230:233], v[192:195], v[102:105]
	v_mfma_f32_16x16x32_bf16 v[94:97], v[238:241], v[192:195], v[94:97]
	v_mfma_f32_16x16x32_bf16 v[86:89], v[230:233], v[200:203], v[86:89]
	v_mfma_f32_16x16x32_bf16 v[78:81], v[238:241], v[200:203], v[78:81]
	v_mfma_f32_16x16x32_bf16 v[70:73], v[230:233], v[208:211], v[70:73]
	v_mfma_f32_16x16x32_bf16 v[58:61], v[238:241], v[208:211], v[58:61]
	s_setprio 0
	s_mov_b32 m0, s41
	v_lshl_add_u64 v[166:167], v[222:223], 0, s[96:97]
	s_barrier
	ds_read_b128 v[180:183], v150 offset:49152
	ds_read_b128 v[184:187], v150 offset:50176
	ds_read_b128 v[188:191], v150 offset:51200
	ds_read_b128 v[192:195], v150 offset:52224
	ds_read_b128 v[196:199], v150 offset:53248
	ds_read_b128 v[200:203], v150 offset:54272
	ds_read_b128 v[204:207], v150 offset:55296
	ds_read_b128 v[208:211], v150 offset:56320
	global_load_lds_dwordx4 v[166:167], off
	v_lshl_add_u64 v[164:165], v[164:165], 0, s[96:97]
	s_mov_b32 m0, s42
	s_nop 0
	global_load_lds_dwordx4 v[164:165], off
	s_barrier
	s_waitcnt lgkmcnt(0)
	s_setprio 1
	s_waitcnt lgkmcnt(0)
	v_mfma_f32_16x16x32_bf16 v[54:57], v[156:159], v[180:183], v[54:57]
	v_mfma_f32_16x16x32_bf16 v[50:53], v[172:175], v[180:183], v[50:53]
	v_mfma_f32_16x16x32_bf16 v[30:33], v[156:159], v[188:191], v[30:33]
	v_mfma_f32_16x16x32_bf16 v[26:29], v[172:175], v[188:191], v[26:29]
	v_mfma_f32_16x16x32_bf16 v[14:17], v[156:159], v[196:199], v[14:17]
	v_mfma_f32_16x16x32_bf16 v[10:13], v[172:175], v[196:199], v[10:13]
	v_mfma_f32_16x16x32_bf16 v[6:9], v[156:159], v[204:207], v[6:9]
	v_mfma_f32_16x16x32_bf16 v[2:5], v[172:175], v[204:207], v[2:5]
	v_mfma_f32_16x16x32_bf16 v[54:57], v[160:163], v[184:187], v[54:57]
	v_mfma_f32_16x16x32_bf16 v[50:53], v[176:179], v[184:187], v[50:53]
	v_mfma_f32_16x16x32_bf16 v[30:33], v[160:163], v[192:195], v[30:33]
	v_mfma_f32_16x16x32_bf16 v[26:29], v[176:179], v[192:195], v[26:29]
	v_mfma_f32_16x16x32_bf16 v[14:17], v[160:163], v[200:203], v[14:17]
	v_mfma_f32_16x16x32_bf16 v[10:13], v[176:179], v[200:203], v[10:13]
	v_mfma_f32_16x16x32_bf16 v[6:9], v[160:163], v[208:211], v[6:9]
	v_mfma_f32_16x16x32_bf16 v[2:5], v[176:179], v[208:211], v[2:5]
	s_setprio 0
	s_barrier
	s_add_u32 s24, s24, 0x40080
	s_addc_u32 s25, s25, 0
	s_add_i32 s26, s26, s36
	v_lshl_add_u64 v[156:157], s[24:25], 0, v[130:131]
	s_mov_b32 m0, s26
	s_nop 0
	global_load_lds_dwordx4 v[156:157], off
	v_lshl_add_u64 v[156:157], s[24:25], 0, v[132:133]
	s_add_i32 m0, s26, 0x2000
	s_nop 0
	global_load_lds_dwordx4 v[156:157], off
	s_waitcnt vmcnt(6)
	s_barrier
	s_setprio 1
	v_mfma_f32_16x16x32_bf16 v[62:65], v[212:215], v[180:183], v[62:65]
	v_mfma_f32_16x16x32_bf16 v[66:69], v[234:237], v[180:183], v[66:69]
	v_mfma_f32_16x16x32_bf16 v[42:45], v[212:215], v[188:191], v[42:45]
	v_mfma_f32_16x16x32_bf16 v[46:49], v[234:237], v[188:191], v[46:49]
	v_mfma_f32_16x16x32_bf16 v[34:37], v[212:215], v[196:199], v[34:37]
	v_mfma_f32_16x16x32_bf16 v[38:41], v[234:237], v[196:199], v[38:41]
	v_mfma_f32_16x16x32_bf16 v[18:21], v[212:215], v[204:207], v[18:21]
	v_mfma_f32_16x16x32_bf16 v[22:25], v[234:237], v[204:207], v[22:25]
	v_mfma_f32_16x16x32_bf16 v[62:65], v[230:233], v[184:187], v[62:65]
	v_mfma_f32_16x16x32_bf16 v[66:69], v[238:241], v[184:187], v[66:69]
	v_mfma_f32_16x16x32_bf16 v[42:45], v[230:233], v[192:195], v[42:45]
	v_mfma_f32_16x16x32_bf16 v[46:49], v[238:241], v[192:195], v[46:49]
	v_mfma_f32_16x16x32_bf16 v[34:37], v[230:233], v[200:203], v[34:37]
	v_mfma_f32_16x16x32_bf16 v[38:41], v[238:241], v[200:203], v[38:41]
	v_mfma_f32_16x16x32_bf16 v[18:21], v[230:233], v[208:211], v[18:21]
	v_mfma_f32_16x16x32_bf16 v[22:25], v[238:241], v[208:211], v[22:25]
	s_setprio 0
	s_add_i32 s49, s49, 2
	s_add_u32 s22, s22, 0x100
	s_addc_u32 s23, s23, 0
	s_cmp_gt_u32 s49, 13
	s_barrier
	s_cbranch_scc0 .LBB0_1327
	v_lshl_add_u32 v136, s46, 8, v135
	v_ashrrev_i32_e32 v137, 31, v136
	v_lshl_add_u64 v[144:145], v[136:137], 2, s[12:13]
	global_load_dword v156, v[144:145], off
	global_load_dword v158, v[144:145], off offset:64
	global_load_dword v160, v[144:145], off offset:128
	global_load_dword v162, v[144:145], off offset:192
	global_load_dword v142, v[144:145], off offset:512
	global_load_dword v140, v[144:145], off offset:576
	global_load_dword v138, v[144:145], off offset:640
	global_load_dword v134, v[144:145], off offset:704
	v_or_b32_e32 v144, 16, v136
	v_or_b32_e32 v164, 32, v136
	v_or_b32_e32 v166, 48, v136
	v_ashrrev_i32_e32 v145, 31, v144
	v_ashrrev_i32_e32 v165, 31, v164
	v_ashrrev_i32_e32 v167, 31, v166
	v_lshl_or_b32 v172, s47, 8, v149
	v_ashrrev_i32_e32 v173, 31, v172
	v_lshlrev_b64 v[136:137], 11, v[136:137]
	v_lshl_add_u64 v[136:137], s[10:11], 0, v[136:137]
	v_lshlrev_b64 v[172:173], 1, v[172:173]
	v_lshl_add_u64 v[136:137], v[136:137], 0, v[172:173]
	s_waitcnt vmcnt(0)
	v_pk_mul_f32 v[128:129], v[128:129], v[156:157] op_sel_hi:[1,0]
	v_pk_mul_f32 v[126:127], v[126:127], v[156:157] op_sel_hi:[1,0]
	v_pk_mul_f32 v[174:175], v[124:125], v[156:157] op_sel_hi:[1,0]
	v_pk_mul_f32 v[124:125], v[122:123], v[156:157] op_sel_hi:[1,0]
	v_cvt_pk_bf16_f32 v122, v126, v127
	v_cvt_pk_bf16_f32 v123, v128, v129
	v_pk_mul_f32 v[120:121], v[120:121], v[156:157] op_sel_hi:[1,0]
	v_cvt_pk_bf16_f32 v124, v124, v125
	v_cvt_pk_bf16_f32 v125, v174, v175
	s_cmp_eq_u32 s101, 1
	s_cbranch_scc1 .Lgs3_a_0
	global_store_dwordx4 v[136:137], v[122:125], off
	s_branch .Lgs3_b_0
.Lgs3_a_0:
	global_store_dwordx4 v[136:137], v[122:125], off sc1
.Lgs3_b_0:
	v_pk_mul_f32 v[118:119], v[118:119], v[156:157] op_sel_hi:[1,0]
	v_pk_mul_f32 v[114:115], v[114:115], v[158:159] op_sel_hi:[1,0]
	v_pk_mul_f32 v[122:123], v[112:113], v[156:157] op_sel_hi:[1,0]
	v_pk_mul_f32 v[112:113], v[110:111], v[156:157] op_sel_hi:[1,0]
	v_cvt_pk_bf16_f32 v110, v118, v119
	v_cvt_pk_bf16_f32 v111, v120, v121
	v_pk_mul_f32 v[104:105], v[104:105], v[158:159] op_sel_hi:[1,0]
	v_cvt_pk_bf16_f32 v112, v112, v113
	v_cvt_pk_bf16_f32 v113, v122, v123
	s_cmp_eq_u32 s101, 1
	s_cbranch_scc1 .Lgs3_a_1
	global_store_dwordx4 v[136:137], v[110:113], off offset:256
	s_branch .Lgs3_b_1
.Lgs3_a_1:
	global_store_dwordx4 v[136:137], v[110:113], off offset:256 sc1
.Lgs3_b_1:
	v_pk_mul_f32 v[102:103], v[102:103], v[158:159] op_sel_hi:[1,0]
	v_pk_mul_f32 v[98:99], v[98:99], v[160:161] op_sel_hi:[1,0]
	v_lshlrev_b64 v[110:111], 11, v[144:145]
	v_lshl_add_u64 v[110:111], s[10:11], 0, v[110:111]
	v_lshl_add_u64 v[110:111], v[110:111], 0, v[172:173]
	v_pk_mul_f32 v[112:113], v[116:117], v[158:159] op_sel_hi:[1,0]
	v_pk_mul_f32 v[116:117], v[108:109], v[158:159] op_sel_hi:[1,0]
	v_pk_mul_f32 v[108:109], v[106:107], v[158:159] op_sel_hi:[1,0]
	v_cvt_pk_bf16_f32 v106, v114, v115
	v_cvt_pk_bf16_f32 v107, v112, v113
	v_pk_mul_f32 v[88:89], v[88:89], v[160:161] op_sel_hi:[1,0]
	v_cvt_pk_bf16_f32 v108, v108, v109
	v_cvt_pk_bf16_f32 v109, v116, v117
	s_cmp_eq_u32 s101, 1
	s_cbranch_scc1 .Lgs3_a_2
	global_store_dwordx4 v[110:111], v[106:109], off
	s_branch .Lgs3_b_2
.Lgs3_a_2:
	global_store_dwordx4 v[110:111], v[106:109], off sc1
.Lgs3_b_2:
	v_pk_mul_f32 v[86:87], v[86:87], v[160:161] op_sel_hi:[1,0]
	v_pk_mul_f32 v[82:83], v[82:83], v[162:163] op_sel_hi:[1,0]
	v_pk_mul_f32 v[106:107], v[96:97], v[158:159] op_sel_hi:[1,0]
	v_pk_mul_f32 v[96:97], v[94:95], v[158:159] op_sel_hi:[1,0]
	v_cvt_pk_bf16_f32 v94, v102, v103
	v_cvt_pk_bf16_f32 v95, v104, v105
	v_pk_mul_f32 v[72:73], v[72:73], v[162:163] op_sel_hi:[1,0]
	v_cvt_pk_bf16_f32 v96, v96, v97
	v_cvt_pk_bf16_f32 v97, v106, v107
	s_cmp_eq_u32 s101, 1
	s_cbranch_scc1 .Lgs3_a_3
	global_store_dwordx4 v[110:111], v[94:97], off offset:256
	s_branch .Lgs3_b_3
.Lgs3_a_3:
	global_store_dwordx4 v[110:111], v[94:97], off offset:256 sc1
.Lgs3_b_3:
	v_pk_mul_f32 v[70:71], v[70:71], v[162:163] op_sel_hi:[1,0]
	v_pk_mul_f32 v[54:55], v[54:55], v[142:143] op_sel_hi:[1,0]
	v_lshlrev_b64 v[94:95], 11, v[164:165]
	v_lshl_add_u64 v[94:95], s[10:11], 0, v[94:95]
	v_lshl_add_u64 v[94:95], v[94:95], 0, v[172:173]
	v_pk_mul_f32 v[96:97], v[100:101], v[160:161] op_sel_hi:[1,0]
	v_pk_mul_f32 v[100:101], v[92:93], v[160:161] op_sel_hi:[1,0]
	v_pk_mul_f32 v[92:93], v[90:91], v[160:161] op_sel_hi:[1,0]
	v_cvt_pk_bf16_f32 v90, v98, v99
	v_cvt_pk_bf16_f32 v91, v96, v97
	s_mov_b32 s6, 0x40000
	v_cvt_pk_bf16_f32 v92, v92, v93
	v_cvt_pk_bf16_f32 v93, v100, v101
	s_cmp_eq_u32 s101, 1
	s_cbranch_scc1 .Lgs3_a_4
	global_store_dwordx4 v[94:95], v[90:93], off
	s_branch .Lgs3_b_4
.Lgs3_a_4:
	global_store_dwordx4 v[94:95], v[90:93], off sc1
.Lgs3_b_4:
	v_pk_mul_f32 v[56:57], v[56:57], v[142:143] op_sel_hi:[1,0]
	v_pk_mul_f32 v[30:31], v[30:31], v[140:141] op_sel_hi:[1,0]
	v_pk_mul_f32 v[90:91], v[80:81], v[160:161] op_sel_hi:[1,0]
	v_pk_mul_f32 v[80:81], v[78:79], v[160:161] op_sel_hi:[1,0]
	v_cvt_pk_bf16_f32 v78, v86, v87
	v_cvt_pk_bf16_f32 v79, v88, v89
	v_pk_mul_f32 v[32:33], v[32:33], v[140:141] op_sel_hi:[1,0]
	v_cvt_pk_bf16_f32 v80, v80, v81
	v_cvt_pk_bf16_f32 v81, v90, v91
	s_cmp_eq_u32 s101, 1
	s_cbranch_scc1 .Lgs3_a_5
	global_store_dwordx4 v[94:95], v[78:81], off offset:256
	s_branch .Lgs3_b_5
.Lgs3_a_5:
	global_store_dwordx4 v[94:95], v[78:81], off offset:256 sc1
.Lgs3_b_5:
	v_pk_mul_f32 v[14:15], v[14:15], v[138:139] op_sel_hi:[1,0]
	v_pk_mul_f32 v[16:17], v[16:17], v[138:139] op_sel_hi:[1,0]
	v_lshlrev_b64 v[78:79], 11, v[166:167]
	v_lshl_add_u64 v[78:79], s[10:11], 0, v[78:79]
	v_lshl_add_u64 v[78:79], v[78:79], 0, v[172:173]
	v_pk_mul_f32 v[80:81], v[84:85], v[162:163] op_sel_hi:[1,0]
	v_pk_mul_f32 v[84:85], v[76:77], v[162:163] op_sel_hi:[1,0]
	v_pk_mul_f32 v[76:77], v[74:75], v[162:163] op_sel_hi:[1,0]
	v_cvt_pk_bf16_f32 v74, v82, v83
	v_cvt_pk_bf16_f32 v75, v80, v81
	v_pk_mul_f32 v[6:7], v[6:7], v[134:135] op_sel_hi:[1,0]
	v_cvt_pk_bf16_f32 v76, v76, v77
	v_cvt_pk_bf16_f32 v77, v84, v85
	s_cmp_eq_u32 s101, 1
	s_cbranch_scc1 .Lgs3_a_6
	global_store_dwordx4 v[78:79], v[74:77], off
	s_branch .Lgs3_b_6
.Lgs3_a_6:
	global_store_dwordx4 v[78:79], v[74:77], off sc1
.Lgs3_b_6:
	v_pk_mul_f32 v[8:9], v[8:9], v[134:135] op_sel_hi:[1,0]
	s_mov_b32 s47, s18
	v_pk_mul_f32 v[74:75], v[60:61], v[162:163] op_sel_hi:[1,0]
	v_pk_mul_f32 v[60:61], v[58:59], v[162:163] op_sel_hi:[1,0]
	v_cvt_pk_bf16_f32 v58, v70, v71
	v_cvt_pk_bf16_f32 v59, v72, v73
	s_mov_b32 s46, s45
	v_cvt_pk_bf16_f32 v60, v60, v61
	v_cvt_pk_bf16_f32 v61, v74, v75
	s_cmp_eq_u32 s101, 1
	s_cbranch_scc1 .Lgs3_a_7
	global_store_dwordx4 v[78:79], v[58:61], off offset:256
	s_branch .Lgs3_b_7
.Lgs3_a_7:
	global_store_dwordx4 v[78:79], v[58:61], off offset:256 sc1
.Lgs3_b_7:
	s_mov_b64 s[22:23], s[20:21]
	s_mov_b32 s49, 0x8000
	v_pk_mul_f32 v[60:61], v[52:53], v[142:143] op_sel_hi:[1,0]
	v_pk_mul_f32 v[52:53], v[50:51], v[142:143] op_sel_hi:[1,0]
	v_cvt_pk_bf16_f32 v50, v54, v55
	v_add_co_u32_e32 v54, vcc, s6, v136
	v_cvt_pk_bf16_f32 v51, v56, v57
	v_cvt_pk_bf16_f32 v52, v52, v53
	v_cvt_pk_bf16_f32 v53, v60, v61
	v_lshl_add_u64 v[58:59], v[136:137], 0, s[94:95]
	s_nop 0
	v_addc_co_u32_e32 v55, vcc, 0, v137, vcc
	s_cmp_eq_u32 s101, 1
	s_cbranch_scc1 .Lgs3_a_8
	global_store_dwordx4 v[54:55], v[50:53], off
	s_branch .Lgs3_b_8

.Lgs3_b_8:
	s_mov_b64 s[6:7], 0x48000
	v_pk_mul_f32 v[54:55], v[68:69], v[142:143] op_sel_hi:[1,0]
	v_pk_mul_f32 v[50:51], v[62:63], v[142:143] op_sel_hi:[1,0]
	v_pk_mul_f32 v[52:53], v[64:65], v[142:143] op_sel_hi:[1,0]
	v_cvt_pk_bf16_f32 v50, v50, v51
	v_pk_mul_f32 v[56:57], v[66:67], v[142:143] op_sel_hi:[1,0]
	v_cvt_pk_bf16_f32 v51, v52, v53
	s_nop 0
	v_cvt_pk_bf16_f32 v52, v56, v57
	v_cvt_pk_bf16_f32 v53, v54, v55
	s_cmp_eq_u32 s101, 1
	s_cbranch_scc1 .Lgs3_a_9
	global_store_dwordx4 v[58:59], v[50:53], off offset:256
	s_branch .Lgs3_b_9
.Lgs3_a_9:
	global_store_dwordx4 v[58:59], v[50:53], off offset:256 sc1
.Lgs3_b_9:
	s_nop 1
	v_lshl_add_u64 v[50:51], v[136:137], 0, s[6:7]
	s_mov_b32 s6, 0x48000
	v_pk_mul_f32 v[52:53], v[28:29], v[140:141] op_sel_hi:[1,0]
	v_pk_mul_f32 v[28:29], v[26:27], v[140:141] op_sel_hi:[1,0]
	v_cvt_pk_bf16_f32 v26, v30, v31
	v_add_co_u32_e32 v30, vcc, s6, v136
	v_cvt_pk_bf16_f32 v27, v32, v33
	v_cvt_pk_bf16_f32 v28, v28, v29
	v_cvt_pk_bf16_f32 v29, v52, v53
	s_mov_b64 s[6:7], 0x50000
	s_nop 0
	v_addc_co_u32_e32 v31, vcc, 0, v137, vcc
	s_cmp_eq_u32 s101, 1
	s_cbranch_scc1 .Lgs3_a_10
	global_store_dwordx4 v[30:31], v[26:29], off
	s_branch .Lgs3_b_10
.Lgs3_a_10:
	global_store_dwordx4 v[30:31], v[26:29], off sc1
.Lgs3_b_10:
	v_pk_mul_f32 v[30:31], v[48:49], v[140:141] op_sel_hi:[1,0]
	v_pk_mul_f32 v[32:33], v[46:47], v[140:141] op_sel_hi:[1,0]
	v_pk_mul_f32 v[26:27], v[42:43], v[140:141] op_sel_hi:[1,0]
	v_pk_mul_f32 v[28:29], v[44:45], v[140:141] op_sel_hi:[1,0]
	v_cvt_pk_bf16_f32 v26, v26, v27
	v_mov_b32_e32 v140, v153
	v_cvt_pk_bf16_f32 v27, v28, v29
	v_cvt_pk_bf16_f32 v28, v32, v33
	v_cvt_pk_bf16_f32 v29, v30, v31
	s_cmp_eq_u32 s101, 1
	s_cbranch_scc1 .Lgs3_a_11
	global_store_dwordx4 v[50:51], v[26:29], off offset:256
	s_branch .Lgs3_b_11
.Lgs3_a_11:
	global_store_dwordx4 v[50:51], v[26:29], off offset:256 sc1
.Lgs3_b_11:
	s_nop 1
	v_lshl_add_u64 v[26:27], v[136:137], 0, s[6:7]
	s_mov_b32 s6, 0x50000
	v_pk_mul_f32 v[28:29], v[12:13], v[138:139] op_sel_hi:[1,0]
	v_pk_mul_f32 v[12:13], v[10:11], v[138:139] op_sel_hi:[1,0]
	v_cvt_pk_bf16_f32 v10, v14, v15
	v_add_co_u32_e32 v14, vcc, s6, v136
	v_cvt_pk_bf16_f32 v11, v16, v17
	v_cvt_pk_bf16_f32 v12, v12, v13
	v_cvt_pk_bf16_f32 v13, v28, v29
	s_mov_b64 s[6:7], 0x58000
	s_nop 0
	v_addc_co_u32_e32 v15, vcc, 0, v137, vcc
	s_cmp_eq_u32 s101, 1
	s_cbranch_scc1 .Lgs3_a_12
	global_store_dwordx4 v[14:15], v[10:13], off
	s_branch .Lgs3_b_12
.Lgs3_a_12:
	global_store_dwordx4 v[14:15], v[10:13], off sc1
.Lgs3_b_12:
	v_pk_mul_f32 v[14:15], v[40:41], v[138:139] op_sel_hi:[1,0]
	v_pk_mul_f32 v[16:17], v[38:39], v[138:139] op_sel_hi:[1,0]
	v_pk_mul_f32 v[10:11], v[34:35], v[138:139] op_sel_hi:[1,0]
	v_pk_mul_f32 v[12:13], v[36:37], v[138:139] op_sel_hi:[1,0]
	v_cvt_pk_bf16_f32 v10, v10, v11
	v_mov_b32_e32 v138, v154
	v_cvt_pk_bf16_f32 v11, v12, v13
	v_cvt_pk_bf16_f32 v12, v16, v17
	v_cvt_pk_bf16_f32 v13, v14, v15
	s_cmp_eq_u32 s101, 1
	s_cbranch_scc1 .Lgs3_a_13
	global_store_dwordx4 v[26:27], v[10:13], off offset:256
	s_branch .Lgs3_b_13
.Lgs3_a_13:
	global_store_dwordx4 v[26:27], v[10:13], off offset:256 sc1
.Lgs3_b_13:
	s_nop 1
	v_lshl_add_u64 v[10:11], v[136:137], 0, s[6:7]
	s_mov_b32 s6, 0x58000
	v_pk_mul_f32 v[12:13], v[4:5], v[134:135] op_sel_hi:[1,0]
	v_pk_mul_f32 v[4:5], v[2:3], v[134:135] op_sel_hi:[1,0]
	v_cvt_pk_bf16_f32 v2, v6, v7
	v_add_co_u32_e32 v6, vcc, s6, v136
	v_cvt_pk_bf16_f32 v3, v8, v9
	v_cvt_pk_bf16_f32 v4, v4, v5
	v_cvt_pk_bf16_f32 v5, v12, v13
	v_pk_mul_f32 v[8:9], v[22:23], v[134:135] op_sel_hi:[1,0]
	s_nop 0
	v_addc_co_u32_e32 v7, vcc, 0, v137, vcc
	s_cmp_eq_u32 s101, 1
	s_cbranch_scc1 .Lgs3_a_14
	global_store_dwordx4 v[6:7], v[2:5], off
	s_branch .Lgs3_b_14

.Lgs3_b_14:
	v_pk_mul_f32 v[6:7], v[24:25], v[134:135] op_sel_hi:[1,0]
	s_and_b64 vcc, exec, s[4:5]
	v_pk_mul_f32 v[4:5], v[20:21], v[134:135] op_sel_hi:[1,0]
	v_pk_mul_f32 v[2:3], v[18:19], v[134:135] op_sel_hi:[1,0]
	v_mov_b32_e32 v136, v152
	v_mov_b32_e32 v134, v151
	v_cvt_pk_bf16_f32 v2, v2, v3
	v_cvt_pk_bf16_f32 v3, v4, v5
	v_cvt_pk_bf16_f32 v4, v8, v9
	v_cvt_pk_bf16_f32 v5, v6, v7
	s_cmp_eq_u32 s101, 1
	s_cbranch_scc1 .Lgs3_a_15
	global_store_dwordx4 v[10:11], v[2:5], off offset:256
	s_branch .Lgs3_b_15

.Lgs3_b_15:
	s_cbranch_vccz .LBB0_1318
	s_waitcnt vmcnt(0)
	s_cmpk_gt_u32 s30, 0xff
	s_cbranch_scc1 .LBB0_1331
	s_barrier
